# speedup vs baseline: 1.0175x; 1.0152x over previous
_Z11pwconv_mfmaPKfPK15HIP_vector_typeIjLj4EES0_Pf:
	s_load_dwordx4 s[12:15], s[0:1], 0x0
	s_load_dwordx4 s[16:19], s[0:1], 0x10
	s_and_b32 s20, s2, 7
	s_lshr_b32 s21, s2, 3
	s_lshr_b32 s37, s20, 1
	s_and_b32 s36, s20, 1
	s_mul_i32 s36, s36, 31
	s_add_i32 s36, s36, s21
	s_lshr_b32 s21, s36, 1
	s_and_b32 s36, s36, 1
	s_lshl_b32 s37, s37, 1
	s_add_i32 s20, s37, s36
	v_lshrrev_b32_e32 v1, 6, v0
	v_and_b32_e32 v2, 63, v0
	s_nop 0
	v_readfirstlane_b32 s22, v1
	s_nop 3
	s_lshl_b32 s23, s20, 3
	s_add_i32 s23, s23, s22
	s_mul_i32 s24, s23, 0x439200
	s_mul_i32 s25, s21, 0x1f0
	s_add_u32 s24, s24, s25
	s_lshl_b32 s25, s21, 17
	s_lshl_b32 s26, s22, 13
	s_add_u32 s25, s25, s26
	s_mul_i32 s27, s20, 0x1e080
	s_mul_i32 s36, s21, 0x1f0
	s_add_u32 s27, s27, s36
	v_min_u32_e32 v10, 61, v2
	v_lshlrev_b32_e32 v3, 3, v10
	v_lshlrev_b32_e32 v4, 4, v2
	v_cmp_lt_u32_e32 vcc, 30, v10
	s_nop 1
	v_cndmask_b32_e64 v5, 0, 1, vcc
	v_mul_u32_u24_e32 v6, 31, v5
	v_sub_u32_e32 v6, v10, v6
	v_lshl_add_u32 v7, v1, 1, v5
	v_and_b32_e32 v8, 7, v6
	v_xor_b32_e32 v7, v7, v8
	v_lshlrev_b32_e32 v7, 4, v7
	v_lshl_add_u32 v5, v6, 12, v7
	s_lshl_b32 s36, s22, 2
	s_add_i32 s36, s36, 0
	s_and_b32 s36, s36, 7
	s_lshl_b32 s37, s22, 14
	s_add_i32 s37, s37, 0x0
	v_xor_b32_e32 v6, s36, v2
	v_lshlrev_b32_e32 v6, 4, v6
	v_add_u32_e32 v6, s37, v6
	s_lshl_b32 s36, s22, 2
	s_add_i32 s36, s36, 1
	s_and_b32 s36, s36, 7
	s_lshl_b32 s37, s22, 14
	s_add_i32 s37, s37, 0x1000
	v_xor_b32_e32 v7, s36, v2
	v_lshlrev_b32_e32 v7, 4, v7
	v_add_u32_e32 v7, s37, v7
	s_lshl_b32 s36, s22, 2
	s_add_i32 s36, s36, 2
	s_and_b32 s36, s36, 7
	s_lshl_b32 s37, s22, 14
	s_add_i32 s37, s37, 0x2000
	v_xor_b32_e32 v8, s36, v2
	v_lshlrev_b32_e32 v8, 4, v8
	v_add_u32_e32 v8, s37, v8
	s_lshl_b32 s36, s22, 2
	s_add_i32 s36, s36, 3
	s_and_b32 s36, s36, 7
	s_lshl_b32 s37, s22, 14
	s_add_i32 s37, s37, 0x3000
	v_xor_b32_e32 v9, s36, v2
	v_lshlrev_b32_e32 v9, 4, v9
	v_add_u32_e32 v9, s37, v9
	v_lshrrev_b32_e32 v10, 5, v0
	v_lshrrev_b32_e32 v11, 1, v10
	v_mul_u32_u24_e32 v11, 0x3c10, v11
	v_and_b32_e32 v10, 1, v10
	v_mul_u32_u24_e32 v10, 0xf8, v10
	v_add_u32_e32 v11, v11, v10
	v_and_b32_e32 v10, 31, v0
	v_lshl_add_u32 v11, v10, 3, v11
	v_add_u32_e32 v11, s27, v11
	v_cmp_eq_u32_e32 vcc, 31, v10
	v_mov_b32_e32 v10, 0x7f000000
	s_nop 1
	v_cndmask_b32_e32 v11, v11, v10, vcc
	s_waitcnt lgkmcnt(0)
	s_add_u32 s4, s12, s24
	s_addc_u32 s5, s13, 0
	s_and_b32 s5, s5, 0xffff
	s_sub_u32 s6, 0x10e48000, s24
	s_mov_b32 s7, 0x20000
	s_add_u32 s8, s14, s25
	s_addc_u32 s9, s15, 0
	s_and_b32 s9, s9, 0xffff
	s_sub_u32 s10, 0x400000, s25
	s_mov_b32 s11, 0x20000
	s_mov_b32 s28, s16
	s_and_b32 s29, s17, 0xffff
	s_mov_b32 s30, 0xf0400
	s_mov_b32 s31, 0x20000
	s_mov_b32 s32, s18
	s_and_b32 s33, s19, 0xffff
	s_mov_b32 s34, 0xf04000
	s_mov_b32 s35, 0x20000
	s_mov_b32 s40, 0x0
	s_mov_b32 s41, 0x21c90
	s_mov_b32 s42, 0x43920
	s_mov_b32 s43, 0x655b0
	s_mov_b32 s44, 0x87240
	s_mov_b32 s45, 0xa8ed0
	s_mov_b32 s46, 0xcab60
	s_mov_b32 s47, 0xec7f0
	buffer_load_dwordx2 v[44:45], v3, s[4:7], s40 offen nt
	buffer_load_dwordx2 v[46:47], v3, s[4:7], s41 offen nt
	buffer_load_dwordx2 v[48:49], v3, s[4:7], s42 offen nt
	buffer_load_dwordx2 v[50:51], v3, s[4:7], s43 offen nt
	buffer_load_dwordx2 v[52:53], v3, s[4:7], s44 offen nt
	buffer_load_dwordx2 v[54:55], v3, s[4:7], s45 offen nt
	buffer_load_dwordx2 v[56:57], v3, s[4:7], s46 offen nt
	buffer_load_dwordx2 v[58:59], v3, s[4:7], s47 offen nt
	s_mov_b32 s40, 0x10e480
	s_mov_b32 s41, 0x130110
	s_mov_b32 s42, 0x151da0
	s_mov_b32 s43, 0x173a30
	s_mov_b32 s44, 0x1956c0
	s_mov_b32 s45, 0x1b7350
	s_mov_b32 s46, 0x1d8fe0
	s_mov_b32 s47, 0x1fac70
	buffer_load_dwordx2 v[60:61], v3, s[4:7], s40 offen nt
	buffer_load_dwordx2 v[62:63], v3, s[4:7], s41 offen nt
	buffer_load_dwordx2 v[64:65], v3, s[4:7], s42 offen nt
	buffer_load_dwordx2 v[66:67], v3, s[4:7], s43 offen nt
	buffer_load_dwordx2 v[68:69], v3, s[4:7], s44 offen nt
	buffer_load_dwordx2 v[70:71], v3, s[4:7], s45 offen nt
	buffer_load_dwordx2 v[72:73], v3, s[4:7], s46 offen nt
	buffer_load_dwordx2 v[74:75], v3, s[4:7], s47 offen nt
	s_mov_b32 s40, 0x21c900
	s_mov_b32 s41, 0x23e590
	s_mov_b32 s42, 0x260220
	s_mov_b32 s43, 0x281eb0
	s_mov_b32 s44, 0x2a3b40
	s_mov_b32 s45, 0x2c57d0
	s_mov_b32 s46, 0x2e7460
	s_mov_b32 s47, 0x3090f0
	buffer_load_dwordx2 v[76:77], v3, s[4:7], s40 offen nt
	buffer_load_dwordx2 v[78:79], v3, s[4:7], s41 offen nt
	buffer_load_dwordx2 v[80:81], v3, s[4:7], s42 offen nt
	buffer_load_dwordx2 v[82:83], v3, s[4:7], s43 offen nt
	buffer_load_dwordx2 v[84:85], v3, s[4:7], s44 offen nt
	buffer_load_dwordx2 v[86:87], v3, s[4:7], s45 offen nt
	buffer_load_dwordx2 v[88:89], v3, s[4:7], s46 offen nt
	buffer_load_dwordx2 v[90:91], v3, s[4:7], s47 offen nt
	s_mov_b32 s40, 0x32ad80
	s_mov_b32 s41, 0x34ca10
	s_mov_b32 s42, 0x36e6a0
	s_mov_b32 s43, 0x390330
	s_mov_b32 s44, 0x3b1fc0
	s_mov_b32 s45, 0x3d3c50
	s_mov_b32 s46, 0x3f58e0
	s_mov_b32 s47, 0x417570
	buffer_load_dwordx2 v[92:93], v3, s[4:7], s40 offen nt
	buffer_load_dwordx2 v[94:95], v3, s[4:7], s41 offen nt
	buffer_load_dwordx2 v[96:97], v3, s[4:7], s42 offen nt
	buffer_load_dwordx2 v[98:99], v3, s[4:7], s43 offen nt
	buffer_load_dwordx2 v[100:101], v3, s[4:7], s44 offen nt
	buffer_load_dwordx2 v[102:103], v3, s[4:7], s45 offen nt
	buffer_load_dwordx2 v[104:105], v3, s[4:7], s46 offen nt
	buffer_load_dwordx2 v[106:107], v3, s[4:7], s47 offen nt
	buffer_load_dwordx2 v[252:253], v11, s[28:31], 0 offen
	s_mov_b32 s40, 0x0
	s_mov_b32 s41, 0x400
	s_mov_b32 s42, 0x800
	s_mov_b32 s43, 0xc00
	s_mov_b32 s44, 0x1000
	buffer_load_dwordx4 v[108:111], v4, s[8:11], s40 offen
	buffer_load_dwordx4 v[112:115], v4, s[8:11], s41 offen
	buffer_load_dwordx4 v[116:119], v4, s[8:11], s42 offen
	buffer_load_dwordx4 v[120:123], v4, s[8:11], s43 offen
	buffer_load_dwordx4 v[124:127], v4, s[8:11], s44 offen
	s_mov_b32 s40, 0x1400
	s_mov_b32 s41, 0x1800
	s_mov_b32 s42, 0x1c00
	s_mov_b32 s43, 0x2000
	s_mov_b32 s44, 0x2400
	buffer_load_dwordx4 v[128:131], v4, s[8:11], s40 offen
	buffer_load_dwordx4 v[132:135], v4, s[8:11], s41 offen
	buffer_load_dwordx4 v[136:139], v4, s[8:11], s42 offen
	buffer_load_dwordx4 v[140:143], v4, s[8:11], s43 offen
	buffer_load_dwordx4 v[144:147], v4, s[8:11], s44 offen
	s_mov_b32 s40, 0x10000
	s_mov_b32 s41, 0x10400
	s_mov_b32 s42, 0x10800
	s_mov_b32 s43, 0x10c00
	s_mov_b32 s44, 0x11000
	buffer_load_dwordx4 v[148:151], v4, s[8:11], s40 offen
	buffer_load_dwordx4 v[152:155], v4, s[8:11], s41 offen
	buffer_load_dwordx4 v[156:159], v4, s[8:11], s42 offen
	buffer_load_dwordx4 v[160:163], v4, s[8:11], s43 offen
	buffer_load_dwordx4 v[164:167], v4, s[8:11], s44 offen
	s_mov_b32 s40, 0x11400
	s_mov_b32 s41, 0x11800
	s_mov_b32 s42, 0x11c00
	s_mov_b32 s43, 0x12000
	s_mov_b32 s44, 0x12400
	buffer_load_dwordx4 v[168:171], v4, s[8:11], s40 offen
	buffer_load_dwordx4 v[172:175], v4, s[8:11], s41 offen
	buffer_load_dwordx4 v[176:179], v4, s[8:11], s42 offen
	buffer_load_dwordx4 v[180:183], v4, s[8:11], s43 offen
	buffer_load_dwordx4 v[184:187], v4, s[8:11], s44 offen
	s_waitcnt vmcnt(45)
	v_cvt_pkrtz_f16_f32 v12, v44, v46
	v_cvt_pkrtz_f16_f32 v13, v48, v50
	v_cvt_pkrtz_f16_f32 v14, v52, v54
	v_cvt_pkrtz_f16_f32 v15, v56, v58
	v_cvt_pkrtz_f16_f32 v16, v45, v47
	v_cvt_pkrtz_f16_f32 v17, v49, v51
	v_cvt_pkrtz_f16_f32 v18, v53, v55
	v_cvt_pkrtz_f16_f32 v19, v57, v59
	s_mov_b32 s40, 0x3c10
	s_mov_b32 s41, 0x258a0
	s_mov_b32 s42, 0x47530
	s_mov_b32 s43, 0x691c0
	s_mov_b32 s44, 0x8ae50
	s_mov_b32 s45, 0xacae0
	s_mov_b32 s46, 0xce770
	s_mov_b32 s47, 0xf0400
	buffer_load_dwordx2 v[44:45], v3, s[4:7], s40 offen nt
	buffer_load_dwordx2 v[46:47], v3, s[4:7], s41 offen nt
	buffer_load_dwordx2 v[48:49], v3, s[4:7], s42 offen nt
	buffer_load_dwordx2 v[50:51], v3, s[4:7], s43 offen nt
	buffer_load_dwordx2 v[52:53], v3, s[4:7], s44 offen nt
	buffer_load_dwordx2 v[54:55], v3, s[4:7], s45 offen nt
	buffer_load_dwordx2 v[56:57], v3, s[4:7], s46 offen nt
	buffer_load_dwordx2 v[58:59], v3, s[4:7], s47 offen nt
	ds_write_b128 v5, v[12:15] offset:0
	ds_write_b128 v5, v[16:19] offset:2048
	s_waitcnt vmcnt(45)
	v_cvt_pkrtz_f16_f32 v12, v60, v62
	v_cvt_pkrtz_f16_f32 v13, v64, v66
	v_cvt_pkrtz_f16_f32 v14, v68, v70
	v_cvt_pkrtz_f16_f32 v15, v72, v74
	v_cvt_pkrtz_f16_f32 v16, v61, v63
	v_cvt_pkrtz_f16_f32 v17, v65, v67
	v_cvt_pkrtz_f16_f32 v18, v69, v71
	v_cvt_pkrtz_f16_f32 v19, v73, v75
	s_mov_b32 s40, 0x112090
	s_mov_b32 s41, 0x133d20
	s_mov_b32 s42, 0x1559b0
	s_mov_b32 s43, 0x177640
	s_mov_b32 s44, 0x1992d0
	s_mov_b32 s45, 0x1baf60
	s_mov_b32 s46, 0x1dcbf0
	s_mov_b32 s47, 0x1fe880
	buffer_load_dwordx2 v[60:61], v3, s[4:7], s40 offen nt
	buffer_load_dwordx2 v[62:63], v3, s[4:7], s41 offen nt
	buffer_load_dwordx2 v[64:65], v3, s[4:7], s42 offen nt
	buffer_load_dwordx2 v[66:67], v3, s[4:7], s43 offen nt
	buffer_load_dwordx2 v[68:69], v3, s[4:7], s44 offen nt
	buffer_load_dwordx2 v[70:71], v3, s[4:7], s45 offen nt
	buffer_load_dwordx2 v[72:73], v3, s[4:7], s46 offen nt
	buffer_load_dwordx2 v[74:75], v3, s[4:7], s47 offen nt
	ds_write_b128 v5, v[12:15] offset:256
	ds_write_b128 v5, v[16:19] offset:2304
	s_waitcnt vmcnt(45)
	v_cvt_pkrtz_f16_f32 v12, v76, v78
	v_cvt_pkrtz_f16_f32 v13, v80, v82
	v_cvt_pkrtz_f16_f32 v14, v84, v86
	v_cvt_pkrtz_f16_f32 v15, v88, v90
	v_cvt_pkrtz_f16_f32 v16, v77, v79
	v_cvt_pkrtz_f16_f32 v17, v81, v83
	v_cvt_pkrtz_f16_f32 v18, v85, v87
	v_cvt_pkrtz_f16_f32 v19, v89, v91
	s_mov_b32 s40, 0x220510
	s_mov_b32 s41, 0x2421a0
	s_mov_b32 s42, 0x263e30
	s_mov_b32 s43, 0x285ac0
	s_mov_b32 s44, 0x2a7750
	s_mov_b32 s45, 0x2c93e0
	s_mov_b32 s46, 0x2eb070
	s_mov_b32 s47, 0x30cd00
	buffer_load_dwordx2 v[76:77], v3, s[4:7], s40 offen nt
	buffer_load_dwordx2 v[78:79], v3, s[4:7], s41 offen nt
	buffer_load_dwordx2 v[80:81], v3, s[4:7], s42 offen nt
	buffer_load_dwordx2 v[82:83], v3, s[4:7], s43 offen nt
	buffer_load_dwordx2 v[84:85], v3, s[4:7], s44 offen nt
	buffer_load_dwordx2 v[86:87], v3, s[4:7], s45 offen nt
	buffer_load_dwordx2 v[88:89], v3, s[4:7], s46 offen nt
	buffer_load_dwordx2 v[90:91], v3, s[4:7], s47 offen nt
	ds_write_b128 v5, v[12:15] offset:512
	ds_write_b128 v5, v[16:19] offset:2560
	s_waitcnt vmcnt(45)
	v_cvt_pkrtz_f16_f32 v12, v92, v94
	v_cvt_pkrtz_f16_f32 v13, v96, v98
	v_cvt_pkrtz_f16_f32 v14, v100, v102
	v_cvt_pkrtz_f16_f32 v15, v104, v106
	v_cvt_pkrtz_f16_f32 v16, v93, v95
	v_cvt_pkrtz_f16_f32 v17, v97, v99
	v_cvt_pkrtz_f16_f32 v18, v101, v103
	v_cvt_pkrtz_f16_f32 v19, v105, v107
	s_mov_b32 s40, 0x32e990
	s_mov_b32 s41, 0x350620
	s_mov_b32 s42, 0x3722b0
	s_mov_b32 s43, 0x393f40
	s_mov_b32 s44, 0x3b5bd0
	s_mov_b32 s45, 0x3d7860
	s_mov_b32 s46, 0x3f94f0
	s_mov_b32 s47, 0x41b180
	buffer_load_dwordx2 v[92:93], v3, s[4:7], s40 offen nt
	buffer_load_dwordx2 v[94:95], v3, s[4:7], s41 offen nt
	buffer_load_dwordx2 v[96:97], v3, s[4:7], s42 offen nt
	buffer_load_dwordx2 v[98:99], v3, s[4:7], s43 offen nt
	buffer_load_dwordx2 v[100:101], v3, s[4:7], s44 offen nt
	buffer_load_dwordx2 v[102:103], v3, s[4:7], s45 offen nt
	buffer_load_dwordx2 v[104:105], v3, s[4:7], s46 offen nt
	buffer_load_dwordx2 v[106:107], v3, s[4:7], s47 offen nt
	ds_write_b128 v5, v[12:15] offset:768
	ds_write_b128 v5, v[16:19] offset:2816
	s_waitcnt lgkmcnt(0)
	s_barrier
	ds_read_b128 v[12:15], v6 offset:0
	ds_read_b128 v[16:19], v6 offset:2048
	ds_read_b128 v[20:23], v7 offset:0
	ds_read_b128 v[24:27], v7 offset:2048
	ds_read_b128 v[28:31], v8 offset:0
	ds_read_b128 v[32:35], v8 offset:2048
	ds_read_b128 v[36:39], v9 offset:0
	ds_read_b128 v[40:43], v9 offset:2048
	s_waitcnt vmcnt(32)
	s_waitcnt lgkmcnt(7)
	v_mfma_f32_16x16x32_f16 v[188:191], v[108:111], v[12:15], 0
	v_mfma_f32_16x16x32_f16 v[220:223], v[148:151], v[12:15], 0
	s_waitcnt lgkmcnt(6)
	v_mfma_f32_16x16x32_f16 v[192:195], v[112:115], v[16:19], 0
	v_mfma_f32_16x16x32_f16 v[224:227], v[152:155], v[16:19], 0
	s_waitcnt lgkmcnt(5)
	v_mfma_f32_16x16x32_f16 v[196:199], v[116:119], v[20:23], 0
	v_mfma_f32_16x16x32_f16 v[228:231], v[156:159], v[20:23], 0
	s_waitcnt lgkmcnt(4)
	v_mfma_f32_16x16x32_f16 v[200:203], v[120:123], v[24:27], 0
	v_mfma_f32_16x16x32_f16 v[232:235], v[160:163], v[24:27], 0
	s_waitcnt lgkmcnt(3)
	v_mfma_f32_16x16x32_f16 v[204:207], v[124:127], v[28:31], 0
	v_mfma_f32_16x16x32_f16 v[236:239], v[164:167], v[28:31], 0
	s_waitcnt lgkmcnt(2)
	v_mfma_f32_16x16x32_f16 v[208:211], v[128:131], v[32:35], 0
	v_mfma_f32_16x16x32_f16 v[240:243], v[168:171], v[32:35], 0
	s_waitcnt lgkmcnt(1)
	v_mfma_f32_16x16x32_f16 v[212:215], v[132:135], v[36:39], 0
	v_mfma_f32_16x16x32_f16 v[244:247], v[172:175], v[36:39], 0
	s_waitcnt lgkmcnt(0)
	v_mfma_f32_16x16x32_f16 v[216:219], v[136:139], v[40:43], 0
	v_mfma_f32_16x16x32_f16 v[248:251], v[176:179], v[40:43], 0
	s_waitcnt vmcnt(24)
	v_cvt_pkrtz_f16_f32 v12, v44, v46
	v_cvt_pkrtz_f16_f32 v13, v48, v50
	v_cvt_pkrtz_f16_f32 v14, v52, v54
	v_cvt_pkrtz_f16_f32 v15, v56, v58
	v_cvt_pkrtz_f16_f32 v16, v45, v47
	v_cvt_pkrtz_f16_f32 v17, v49, v51
	v_cvt_pkrtz_f16_f32 v18, v53, v55
	v_cvt_pkrtz_f16_f32 v19, v57, v59
	s_mov_b32 s40, 0x7820
	s_mov_b32 s41, 0x294b0
	s_mov_b32 s42, 0x4b140
	s_mov_b32 s43, 0x6cdd0
	s_mov_b32 s44, 0x8ea60
	s_mov_b32 s45, 0xb06f0
	s_mov_b32 s46, 0xd2380
	s_mov_b32 s47, 0xf4010
	buffer_load_dwordx2 v[44:45], v3, s[4:7], s40 offen nt
	buffer_load_dwordx2 v[46:47], v3, s[4:7], s41 offen nt
	buffer_load_dwordx2 v[48:49], v3, s[4:7], s42 offen nt
	buffer_load_dwordx2 v[50:51], v3, s[4:7], s43 offen nt
	buffer_load_dwordx2 v[52:53], v3, s[4:7], s44 offen nt
	buffer_load_dwordx2 v[54:55], v3, s[4:7], s45 offen nt
	buffer_load_dwordx2 v[56:57], v3, s[4:7], s46 offen nt
	buffer_load_dwordx2 v[58:59], v3, s[4:7], s47 offen nt
	ds_write_b128 v5, v[12:15] offset:1024
	ds_write_b128 v5, v[16:19] offset:3072
	s_waitcnt vmcnt(24)
	v_cvt_pkrtz_f16_f32 v12, v60, v62
	v_cvt_pkrtz_f16_f32 v13, v64, v66
	v_cvt_pkrtz_f16_f32 v14, v68, v70
	v_cvt_pkrtz_f16_f32 v15, v72, v74
	v_cvt_pkrtz_f16_f32 v16, v61, v63
	v_cvt_pkrtz_f16_f32 v17, v65, v67
	v_cvt_pkrtz_f16_f32 v18, v69, v71
	v_cvt_pkrtz_f16_f32 v19, v73, v75
	s_mov_b32 s40, 0x115ca0
	s_mov_b32 s41, 0x137930
	s_mov_b32 s42, 0x1595c0
	s_mov_b32 s43, 0x17b250
	s_mov_b32 s44, 0x19cee0
	s_mov_b32 s45, 0x1beb70
	s_mov_b32 s46, 0x1e0800
	s_mov_b32 s47, 0x202490
	buffer_load_dwordx2 v[60:61], v3, s[4:7], s40 offen nt
	buffer_load_dwordx2 v[62:63], v3, s[4:7], s41 offen nt
	buffer_load_dwordx2 v[64:65], v3, s[4:7], s42 offen nt
	buffer_load_dwordx2 v[66:67], v3, s[4:7], s43 offen nt
	buffer_load_dwordx2 v[68:69], v3, s[4:7], s44 offen nt
	buffer_load_dwordx2 v[70:71], v3, s[4:7], s45 offen nt
	buffer_load_dwordx2 v[72:73], v3, s[4:7], s46 offen nt
	buffer_load_dwordx2 v[74:75], v3, s[4:7], s47 offen nt
	ds_write_b128 v5, v[12:15] offset:1280
	ds_write_b128 v5, v[16:19] offset:3328
	s_waitcnt vmcnt(24)
	v_cvt_pkrtz_f16_f32 v12, v76, v78
	v_cvt_pkrtz_f16_f32 v13, v80, v82
	v_cvt_pkrtz_f16_f32 v14, v84, v86
	v_cvt_pkrtz_f16_f32 v15, v88, v90
	v_cvt_pkrtz_f16_f32 v16, v77, v79
	v_cvt_pkrtz_f16_f32 v17, v81, v83
	v_cvt_pkrtz_f16_f32 v18, v85, v87
	v_cvt_pkrtz_f16_f32 v19, v89, v91
	s_mov_b32 s40, 0x224120
	s_mov_b32 s41, 0x245db0
	s_mov_b32 s42, 0x267a40
	s_mov_b32 s43, 0x2896d0
	s_mov_b32 s44, 0x2ab360
	s_mov_b32 s45, 0x2ccff0
	s_mov_b32 s46, 0x2eec80
	s_mov_b32 s47, 0x310910
	buffer_load_dwordx2 v[76:77], v3, s[4:7], s40 offen nt
	buffer_load_dwordx2 v[78:79], v3, s[4:7], s41 offen nt
	buffer_load_dwordx2 v[80:81], v3, s[4:7], s42 offen nt
	buffer_load_dwordx2 v[82:83], v3, s[4:7], s43 offen nt
	buffer_load_dwordx2 v[84:85], v3, s[4:7], s44 offen nt
	buffer_load_dwordx2 v[86:87], v3, s[4:7], s45 offen nt
	buffer_load_dwordx2 v[88:89], v3, s[4:7], s46 offen nt
	buffer_load_dwordx2 v[90:91], v3, s[4:7], s47 offen nt
	ds_write_b128 v5, v[12:15] offset:1536
	ds_write_b128 v5, v[16:19] offset:3584
	s_waitcnt vmcnt(24)
	v_cvt_pkrtz_f16_f32 v12, v92, v94
	v_cvt_pkrtz_f16_f32 v13, v96, v98
	v_cvt_pkrtz_f16_f32 v14, v100, v102
	v_cvt_pkrtz_f16_f32 v15, v104, v106
	v_cvt_pkrtz_f16_f32 v16, v93, v95
	v_cvt_pkrtz_f16_f32 v17, v97, v99
	v_cvt_pkrtz_f16_f32 v18, v101, v103
	v_cvt_pkrtz_f16_f32 v19, v105, v107
	s_mov_b32 s40, 0x3325a0
	s_mov_b32 s41, 0x354230
	s_mov_b32 s42, 0x375ec0
	s_mov_b32 s43, 0x397b50
	s_mov_b32 s44, 0x3b97e0
	s_mov_b32 s45, 0x3db470
	s_mov_b32 s46, 0x3fd100
	s_mov_b32 s47, 0x41ed90
	buffer_load_dwordx2 v[92:93], v3, s[4:7], s40 offen nt
	buffer_load_dwordx2 v[94:95], v3, s[4:7], s41 offen nt
	buffer_load_dwordx2 v[96:97], v3, s[4:7], s42 offen nt
	buffer_load_dwordx2 v[98:99], v3, s[4:7], s43 offen nt
	buffer_load_dwordx2 v[100:101], v3, s[4:7], s44 offen nt
	buffer_load_dwordx2 v[102:103], v3, s[4:7], s45 offen nt
	buffer_load_dwordx2 v[104:105], v3, s[4:7], s46 offen nt
	buffer_load_dwordx2 v[106:107], v3, s[4:7], s47 offen nt
	ds_write_b128 v5, v[12:15] offset:1792
	ds_write_b128 v5, v[16:19] offset:3840
	s_waitcnt lgkmcnt(0)
	s_barrier
	ds_read_b128 v[12:15], v6 offset:1024
	ds_read_b128 v[16:19], v6 offset:3072
	ds_read_b128 v[20:23], v7 offset:1024
	ds_read_b128 v[24:27], v7 offset:3072
	ds_read_b128 v[28:31], v8 offset:1024
	ds_read_b128 v[32:35], v8 offset:3072
	ds_read_b128 v[36:39], v9 offset:1024
	ds_read_b128 v[40:43], v9 offset:3072
	s_waitcnt lgkmcnt(7)
	v_mfma_f32_16x16x32_f16 v[188:191], v[112:115], v[12:15], v[188:191]
	v_mfma_f32_16x16x32_f16 v[220:223], v[152:155], v[12:15], v[220:223]
	s_waitcnt lgkmcnt(6)
	v_mfma_f32_16x16x32_f16 v[192:195], v[116:119], v[16:19], v[192:195]
	v_mfma_f32_16x16x32_f16 v[224:227], v[156:159], v[16:19], v[224:227]
	s_waitcnt lgkmcnt(5)
	v_mfma_f32_16x16x32_f16 v[196:199], v[120:123], v[20:23], v[196:199]
	v_mfma_f32_16x16x32_f16 v[228:231], v[160:163], v[20:23], v[228:231]
	s_waitcnt lgkmcnt(4)
	v_mfma_f32_16x16x32_f16 v[200:203], v[124:127], v[24:27], v[200:203]
	v_mfma_f32_16x16x32_f16 v[232:235], v[164:167], v[24:27], v[232:235]
	s_waitcnt lgkmcnt(3)
	v_mfma_f32_16x16x32_f16 v[204:207], v[128:131], v[28:31], v[204:207]
	v_mfma_f32_16x16x32_f16 v[236:239], v[168:171], v[28:31], v[236:239]
	s_waitcnt lgkmcnt(2)
	v_mfma_f32_16x16x32_f16 v[208:211], v[132:135], v[32:35], v[208:211]
	v_mfma_f32_16x16x32_f16 v[240:243], v[172:175], v[32:35], v[240:243]
	s_waitcnt lgkmcnt(1)
	v_mfma_f32_16x16x32_f16 v[212:215], v[136:139], v[36:39], v[212:215]
	v_mfma_f32_16x16x32_f16 v[244:247], v[176:179], v[36:39], v[244:247]
	s_waitcnt lgkmcnt(0)
	v_mfma_f32_16x16x32_f16 v[216:219], v[140:143], v[40:43], v[216:219]
	v_mfma_f32_16x16x32_f16 v[248:251], v[180:183], v[40:43], v[248:251]
	s_waitcnt vmcnt(24)
	v_cvt_pkrtz_f16_f32 v12, v44, v46
	v_cvt_pkrtz_f16_f32 v13, v48, v50
	v_cvt_pkrtz_f16_f32 v14, v52, v54
	v_cvt_pkrtz_f16_f32 v15, v56, v58
	v_cvt_pkrtz_f16_f32 v16, v45, v47
	v_cvt_pkrtz_f16_f32 v17, v49, v51
	v_cvt_pkrtz_f16_f32 v18, v53, v55
	v_cvt_pkrtz_f16_f32 v19, v57, v59
	s_mov_b32 s40, 0xb430
	s_mov_b32 s41, 0x2d0c0
	s_mov_b32 s42, 0x4ed50
	s_mov_b32 s43, 0x709e0
	s_mov_b32 s44, 0x92670
	s_mov_b32 s45, 0xb4300
	s_mov_b32 s46, 0xd5f90
	s_mov_b32 s47, 0xf7c20
	buffer_load_dwordx2 v[44:45], v3, s[4:7], s40 offen nt
	buffer_load_dwordx2 v[46:47], v3, s[4:7], s41 offen nt
	buffer_load_dwordx2 v[48:49], v3, s[4:7], s42 offen nt
	buffer_load_dwordx2 v[50:51], v3, s[4:7], s43 offen nt
	buffer_load_dwordx2 v[52:53], v3, s[4:7], s44 offen nt
	buffer_load_dwordx2 v[54:55], v3, s[4:7], s45 offen nt
	buffer_load_dwordx2 v[56:57], v3, s[4:7], s46 offen nt
	buffer_load_dwordx2 v[58:59], v3, s[4:7], s47 offen nt
	ds_write_b128 v5, v[12:15] offset:0
	ds_write_b128 v5, v[16:19] offset:2048
	s_waitcnt vmcnt(24)
	v_cvt_pkrtz_f16_f32 v12, v60, v62
	v_cvt_pkrtz_f16_f32 v13, v64, v66
	v_cvt_pkrtz_f16_f32 v14, v68, v70
	v_cvt_pkrtz_f16_f32 v15, v72, v74
	v_cvt_pkrtz_f16_f32 v16, v61, v63
	v_cvt_pkrtz_f16_f32 v17, v65, v67
	v_cvt_pkrtz_f16_f32 v18, v69, v71
	v_cvt_pkrtz_f16_f32 v19, v73, v75
	s_mov_b32 s40, 0x1198b0
	s_mov_b32 s41, 0x13b540
	s_mov_b32 s42, 0x15d1d0
	s_mov_b32 s43, 0x17ee60
	s_mov_b32 s44, 0x1a0af0
	s_mov_b32 s45, 0x1c2780
	s_mov_b32 s46, 0x1e4410
	s_mov_b32 s47, 0x2060a0
	buffer_load_dwordx2 v[60:61], v3, s[4:7], s40 offen nt
	buffer_load_dwordx2 v[62:63], v3, s[4:7], s41 offen nt
	buffer_load_dwordx2 v[64:65], v3, s[4:7], s42 offen nt
	buffer_load_dwordx2 v[66:67], v3, s[4:7], s43 offen nt
	buffer_load_dwordx2 v[68:69], v3, s[4:7], s44 offen nt
	buffer_load_dwordx2 v[70:71], v3, s[4:7], s45 offen nt
	buffer_load_dwordx2 v[72:73], v3, s[4:7], s46 offen nt
	buffer_load_dwordx2 v[74:75], v3, s[4:7], s47 offen nt
	ds_write_b128 v5, v[12:15] offset:256
	ds_write_b128 v5, v[16:19] offset:2304
	s_waitcnt vmcnt(24)
	v_cvt_pkrtz_f16_f32 v12, v76, v78
	v_cvt_pkrtz_f16_f32 v13, v80, v82
	v_cvt_pkrtz_f16_f32 v14, v84, v86
	v_cvt_pkrtz_f16_f32 v15, v88, v90
	v_cvt_pkrtz_f16_f32 v16, v77, v79
	v_cvt_pkrtz_f16_f32 v17, v81, v83
	v_cvt_pkrtz_f16_f32 v18, v85, v87
	v_cvt_pkrtz_f16_f32 v19, v89, v91
	s_mov_b32 s40, 0x227d30
	s_mov_b32 s41, 0x2499c0
	s_mov_b32 s42, 0x26b650
	s_mov_b32 s43, 0x28d2e0
	s_mov_b32 s44, 0x2aef70
	s_mov_b32 s45, 0x2d0c00
	s_mov_b32 s46, 0x2f2890
	s_mov_b32 s47, 0x314520
	buffer_load_dwordx2 v[76:77], v3, s[4:7], s40 offen nt
	buffer_load_dwordx2 v[78:79], v3, s[4:7], s41 offen nt
	buffer_load_dwordx2 v[80:81], v3, s[4:7], s42 offen nt
	buffer_load_dwordx2 v[82:83], v3, s[4:7], s43 offen nt
	buffer_load_dwordx2 v[84:85], v3, s[4:7], s44 offen nt
	buffer_load_dwordx2 v[86:87], v3, s[4:7], s45 offen nt
	buffer_load_dwordx2 v[88:89], v3, s[4:7], s46 offen nt
	buffer_load_dwordx2 v[90:91], v3, s[4:7], s47 offen nt
	ds_write_b128 v5, v[12:15] offset:512
	ds_write_b128 v5, v[16:19] offset:2560
	s_waitcnt vmcnt(24)
	v_cvt_pkrtz_f16_f32 v12, v92, v94
	v_cvt_pkrtz_f16_f32 v13, v96, v98
	v_cvt_pkrtz_f16_f32 v14, v100, v102
	v_cvt_pkrtz_f16_f32 v15, v104, v106
	v_cvt_pkrtz_f16_f32 v16, v93, v95
	v_cvt_pkrtz_f16_f32 v17, v97, v99
	v_cvt_pkrtz_f16_f32 v18, v101, v103
	v_cvt_pkrtz_f16_f32 v19, v105, v107
	s_mov_b32 s40, 0x3361b0
	s_mov_b32 s41, 0x357e40
	s_mov_b32 s42, 0x379ad0
	s_mov_b32 s43, 0x39b760
	s_mov_b32 s44, 0x3bd3f0
	s_mov_b32 s45, 0x3df080
	s_mov_b32 s46, 0x400d10
	s_mov_b32 s47, 0x4229a0
	buffer_load_dwordx2 v[92:93], v3, s[4:7], s40 offen nt
	buffer_load_dwordx2 v[94:95], v3, s[4:7], s41 offen nt
	buffer_load_dwordx2 v[96:97], v3, s[4:7], s42 offen nt
	buffer_load_dwordx2 v[98:99], v3, s[4:7], s43 offen nt
	buffer_load_dwordx2 v[100:101], v3, s[4:7], s44 offen nt
	buffer_load_dwordx2 v[102:103], v3, s[4:7], s45 offen nt
	buffer_load_dwordx2 v[104:105], v3, s[4:7], s46 offen nt
	buffer_load_dwordx2 v[106:107], v3, s[4:7], s47 offen nt
	ds_write_b128 v5, v[12:15] offset:768
	ds_write_b128 v5, v[16:19] offset:2816
	s_waitcnt lgkmcnt(0)
	s_barrier
	ds_read_b128 v[12:15], v6 offset:0
	ds_read_b128 v[16:19], v6 offset:2048
	ds_read_b128 v[20:23], v7 offset:0
	ds_read_b128 v[24:27], v7 offset:2048
	ds_read_b128 v[28:31], v8 offset:0
	ds_read_b128 v[32:35], v8 offset:2048
	ds_read_b128 v[36:39], v9 offset:0
	ds_read_b128 v[40:43], v9 offset:2048
	s_waitcnt lgkmcnt(7)
	v_mfma_f32_16x16x32_f16 v[188:191], v[116:119], v[12:15], v[188:191]
	v_mfma_f32_16x16x32_f16 v[220:223], v[156:159], v[12:15], v[220:223]
	s_waitcnt lgkmcnt(6)
	v_mfma_f32_16x16x32_f16 v[192:195], v[120:123], v[16:19], v[192:195]
	v_mfma_f32_16x16x32_f16 v[224:227], v[160:163], v[16:19], v[224:227]
	s_waitcnt lgkmcnt(5)
	v_mfma_f32_16x16x32_f16 v[196:199], v[124:127], v[20:23], v[196:199]
	v_mfma_f32_16x16x32_f16 v[228:231], v[164:167], v[20:23], v[228:231]
	s_waitcnt lgkmcnt(4)
	v_mfma_f32_16x16x32_f16 v[200:203], v[128:131], v[24:27], v[200:203]
	v_mfma_f32_16x16x32_f16 v[232:235], v[168:171], v[24:27], v[232:235]
	s_waitcnt lgkmcnt(3)
	v_mfma_f32_16x16x32_f16 v[204:207], v[132:135], v[28:31], v[204:207]
	v_mfma_f32_16x16x32_f16 v[236:239], v[172:175], v[28:31], v[236:239]
	s_waitcnt lgkmcnt(2)
	v_mfma_f32_16x16x32_f16 v[208:211], v[136:139], v[32:35], v[208:211]
	v_mfma_f32_16x16x32_f16 v[240:243], v[176:179], v[32:35], v[240:243]
	s_waitcnt lgkmcnt(1)
	v_mfma_f32_16x16x32_f16 v[212:215], v[140:143], v[36:39], v[212:215]
	v_mfma_f32_16x16x32_f16 v[244:247], v[180:183], v[36:39], v[244:247]
	s_waitcnt lgkmcnt(0)
	v_mfma_f32_16x16x32_f16 v[216:219], v[144:147], v[40:43], v[216:219]
	v_mfma_f32_16x16x32_f16 v[248:251], v[184:187], v[40:43], v[248:251]
	s_mov_b32 s40, 0x20000
	s_mov_b32 s41, 0x20400
	s_mov_b32 s42, 0x20800
	s_mov_b32 s43, 0x20c00
	s_mov_b32 s44, 0x21000
	buffer_load_dwordx4 v[108:111], v4, s[8:11], s40 offen
	buffer_load_dwordx4 v[112:115], v4, s[8:11], s41 offen
	buffer_load_dwordx4 v[116:119], v4, s[8:11], s42 offen
	buffer_load_dwordx4 v[120:123], v4, s[8:11], s43 offen
	buffer_load_dwordx4 v[124:127], v4, s[8:11], s44 offen
	s_mov_b32 s40, 0x21400
	s_mov_b32 s41, 0x21800
	s_mov_b32 s42, 0x21c00
	s_mov_b32 s43, 0x22000
	s_mov_b32 s44, 0x22400
	buffer_load_dwordx4 v[128:131], v4, s[8:11], s40 offen
	buffer_load_dwordx4 v[132:135], v4, s[8:11], s41 offen
	buffer_load_dwordx4 v[136:139], v4, s[8:11], s42 offen
	buffer_load_dwordx4 v[140:143], v4, s[8:11], s43 offen
	buffer_load_dwordx4 v[144:147], v4, s[8:11], s44 offen
	s_waitcnt vmcnt(34)
	v_cvt_pkrtz_f16_f32 v12, v44, v46
	v_cvt_pkrtz_f16_f32 v13, v48, v50
	v_cvt_pkrtz_f16_f32 v14, v52, v54
	v_cvt_pkrtz_f16_f32 v15, v56, v58
	v_cvt_pkrtz_f16_f32 v16, v45, v47
	v_cvt_pkrtz_f16_f32 v17, v49, v51
	v_cvt_pkrtz_f16_f32 v18, v53, v55
	v_cvt_pkrtz_f16_f32 v19, v57, v59
	s_mov_b32 s40, 0xf040
	s_mov_b32 s41, 0x30cd0
	s_mov_b32 s42, 0x52960
	s_mov_b32 s43, 0x745f0
	s_mov_b32 s44, 0x96280
	s_mov_b32 s45, 0xb7f10
	s_mov_b32 s46, 0xd9ba0
	s_mov_b32 s47, 0xfb830
	buffer_load_dwordx2 v[44:45], v3, s[4:7], s40 offen nt
	buffer_load_dwordx2 v[46:47], v3, s[4:7], s41 offen nt
	buffer_load_dwordx2 v[48:49], v3, s[4:7], s42 offen nt
	buffer_load_dwordx2 v[50:51], v3, s[4:7], s43 offen nt
	buffer_load_dwordx2 v[52:53], v3, s[4:7], s44 offen nt
	buffer_load_dwordx2 v[54:55], v3, s[4:7], s45 offen nt
	buffer_load_dwordx2 v[56:57], v3, s[4:7], s46 offen nt
	buffer_load_dwordx2 v[58:59], v3, s[4:7], s47 offen nt
	ds_write_b128 v5, v[12:15] offset:1024
	ds_write_b128 v5, v[16:19] offset:3072
	s_waitcnt vmcnt(34)
	v_cvt_pkrtz_f16_f32 v12, v60, v62
	v_cvt_pkrtz_f16_f32 v13, v64, v66
	v_cvt_pkrtz_f16_f32 v14, v68, v70
	v_cvt_pkrtz_f16_f32 v15, v72, v74
	v_cvt_pkrtz_f16_f32 v16, v61, v63
	v_cvt_pkrtz_f16_f32 v17, v65, v67
	v_cvt_pkrtz_f16_f32 v18, v69, v71
	v_cvt_pkrtz_f16_f32 v19, v73, v75
	s_mov_b32 s40, 0x11d4c0
	s_mov_b32 s41, 0x13f150
	s_mov_b32 s42, 0x160de0
	s_mov_b32 s43, 0x182a70
	s_mov_b32 s44, 0x1a4700
	s_mov_b32 s45, 0x1c6390
	s_mov_b32 s46, 0x1e8020
	s_mov_b32 s47, 0x209cb0
	buffer_load_dwordx2 v[60:61], v3, s[4:7], s40 offen nt
	buffer_load_dwordx2 v[62:63], v3, s[4:7], s41 offen nt
	buffer_load_dwordx2 v[64:65], v3, s[4:7], s42 offen nt
	buffer_load_dwordx2 v[66:67], v3, s[4:7], s43 offen nt
	buffer_load_dwordx2 v[68:69], v3, s[4:7], s44 offen nt
	buffer_load_dwordx2 v[70:71], v3, s[4:7], s45 offen nt
	buffer_load_dwordx2 v[72:73], v3, s[4:7], s46 offen nt
	buffer_load_dwordx2 v[74:75], v3, s[4:7], s47 offen nt
	ds_write_b128 v5, v[12:15] offset:1280
	ds_write_b128 v5, v[16:19] offset:3328
	s_waitcnt vmcnt(34)
	v_cvt_pkrtz_f16_f32 v12, v76, v78
	v_cvt_pkrtz_f16_f32 v13, v80, v82
	v_cvt_pkrtz_f16_f32 v14, v84, v86
	v_cvt_pkrtz_f16_f32 v15, v88, v90
	v_cvt_pkrtz_f16_f32 v16, v77, v79
	v_cvt_pkrtz_f16_f32 v17, v81, v83
	v_cvt_pkrtz_f16_f32 v18, v85, v87
	v_cvt_pkrtz_f16_f32 v19, v89, v91
	s_mov_b32 s40, 0x22b940
	s_mov_b32 s41, 0x24d5d0
	s_mov_b32 s42, 0x26f260
	s_mov_b32 s43, 0x290ef0
	s_mov_b32 s44, 0x2b2b80
	s_mov_b32 s45, 0x2d4810
	s_mov_b32 s46, 0x2f64a0
	s_mov_b32 s47, 0x318130
	buffer_load_dwordx2 v[76:77], v3, s[4:7], s40 offen nt
	buffer_load_dwordx2 v[78:79], v3, s[4:7], s41 offen nt
	buffer_load_dwordx2 v[80:81], v3, s[4:7], s42 offen nt
	buffer_load_dwordx2 v[82:83], v3, s[4:7], s43 offen nt
	buffer_load_dwordx2 v[84:85], v3, s[4:7], s44 offen nt
	buffer_load_dwordx2 v[86:87], v3, s[4:7], s45 offen nt
	buffer_load_dwordx2 v[88:89], v3, s[4:7], s46 offen nt
	buffer_load_dwordx2 v[90:91], v3, s[4:7], s47 offen nt
	ds_write_b128 v5, v[12:15] offset:1536
	ds_write_b128 v5, v[16:19] offset:3584
	s_waitcnt vmcnt(34)
	v_cvt_pkrtz_f16_f32 v12, v92, v94
	v_cvt_pkrtz_f16_f32 v13, v96, v98
	v_cvt_pkrtz_f16_f32 v14, v100, v102
	v_cvt_pkrtz_f16_f32 v15, v104, v106
	v_cvt_pkrtz_f16_f32 v16, v93, v95
	v_cvt_pkrtz_f16_f32 v17, v97, v99
	v_cvt_pkrtz_f16_f32 v18, v101, v103
	v_cvt_pkrtz_f16_f32 v19, v105, v107
	s_mov_b32 s40, 0x339dc0
	s_mov_b32 s41, 0x35ba50
	s_mov_b32 s42, 0x37d6e0
	s_mov_b32 s43, 0x39f370
	s_mov_b32 s44, 0x3c1000
	s_mov_b32 s45, 0x3e2c90
	s_mov_b32 s46, 0x404920
	s_mov_b32 s47, 0x4265b0
	buffer_load_dwordx2 v[92:93], v3, s[4:7], s40 offen nt
	buffer_load_dwordx2 v[94:95], v3, s[4:7], s41 offen nt
	buffer_load_dwordx2 v[96:97], v3, s[4:7], s42 offen nt
	buffer_load_dwordx2 v[98:99], v3, s[4:7], s43 offen nt
	buffer_load_dwordx2 v[100:101], v3, s[4:7], s44 offen nt
	buffer_load_dwordx2 v[102:103], v3, s[4:7], s45 offen nt
	buffer_load_dwordx2 v[104:105], v3, s[4:7], s46 offen nt
	buffer_load_dwordx2 v[106:107], v3, s[4:7], s47 offen nt
	ds_write_b128 v5, v[12:15] offset:1792
	ds_write_b128 v5, v[16:19] offset:3840
	s_waitcnt lgkmcnt(0)
	s_barrier
	ds_read_b128 v[12:15], v6 offset:1024
	ds_read_b128 v[16:19], v6 offset:3072
	ds_read_b128 v[20:23], v7 offset:1024
	ds_read_b128 v[24:27], v7 offset:3072
	ds_read_b128 v[28:31], v8 offset:1024
	ds_read_b128 v[32:35], v8 offset:3072
	ds_read_b128 v[36:39], v9 offset:1024
	ds_read_b128 v[40:43], v9 offset:3072
	s_waitcnt vmcnt(32)
	s_waitcnt lgkmcnt(7)
	v_mfma_f32_16x16x32_f16 v[188:191], v[148:151], v[12:15], v[188:191]
	v_mfma_f32_16x16x32_f16 v[220:223], v[108:111], v[12:15], v[220:223]
	s_waitcnt lgkmcnt(6)
	v_mfma_f32_16x16x32_f16 v[192:195], v[152:155], v[16:19], v[192:195]
	v_mfma_f32_16x16x32_f16 v[224:227], v[112:115], v[16:19], v[224:227]
	s_waitcnt lgkmcnt(5)
	v_mfma_f32_16x16x32_f16 v[196:199], v[156:159], v[20:23], v[196:199]
	v_mfma_f32_16x16x32_f16 v[228:231], v[116:119], v[20:23], v[228:231]
	s_waitcnt lgkmcnt(4)
	v_mfma_f32_16x16x32_f16 v[200:203], v[160:163], v[24:27], v[200:203]
	v_mfma_f32_16x16x32_f16 v[232:235], v[120:123], v[24:27], v[232:235]
	s_waitcnt lgkmcnt(3)
	v_mfma_f32_16x16x32_f16 v[204:207], v[164:167], v[28:31], v[204:207]
	v_mfma_f32_16x16x32_f16 v[236:239], v[124:127], v[28:31], v[236:239]
	s_waitcnt lgkmcnt(2)
	v_mfma_f32_16x16x32_f16 v[208:211], v[168:171], v[32:35], v[208:211]
	v_mfma_f32_16x16x32_f16 v[240:243], v[128:131], v[32:35], v[240:243]
	s_waitcnt lgkmcnt(1)
	v_mfma_f32_16x16x32_f16 v[212:215], v[172:175], v[36:39], v[212:215]
	v_mfma_f32_16x16x32_f16 v[244:247], v[132:135], v[36:39], v[244:247]
	s_waitcnt lgkmcnt(0)
	v_mfma_f32_16x16x32_f16 v[216:219], v[176:179], v[40:43], v[216:219]
	v_mfma_f32_16x16x32_f16 v[248:251], v[136:139], v[40:43], v[248:251]
	s_waitcnt vmcnt(24)
	v_cvt_pkrtz_f16_f32 v12, v44, v46
	v_cvt_pkrtz_f16_f32 v13, v48, v50
	v_cvt_pkrtz_f16_f32 v14, v52, v54
	v_cvt_pkrtz_f16_f32 v15, v56, v58
	v_cvt_pkrtz_f16_f32 v16, v45, v47
	v_cvt_pkrtz_f16_f32 v17, v49, v51
	v_cvt_pkrtz_f16_f32 v18, v53, v55
	v_cvt_pkrtz_f16_f32 v19, v57, v59
	s_mov_b32 s40, 0x12c50
	s_mov_b32 s41, 0x348e0
	s_mov_b32 s42, 0x56570
	s_mov_b32 s43, 0x78200
	s_mov_b32 s44, 0x99e90
	s_mov_b32 s45, 0xbbb20
	s_mov_b32 s46, 0xdd7b0
	s_mov_b32 s47, 0xff440
	buffer_load_dwordx2 v[44:45], v3, s[4:7], s40 offen nt
	buffer_load_dwordx2 v[46:47], v3, s[4:7], s41 offen nt
	buffer_load_dwordx2 v[48:49], v3, s[4:7], s42 offen nt
	buffer_load_dwordx2 v[50:51], v3, s[4:7], s43 offen nt
	buffer_load_dwordx2 v[52:53], v3, s[4:7], s44 offen nt
	buffer_load_dwordx2 v[54:55], v3, s[4:7], s45 offen nt
	buffer_load_dwordx2 v[56:57], v3, s[4:7], s46 offen nt
	buffer_load_dwordx2 v[58:59], v3, s[4:7], s47 offen nt
	ds_write_b128 v5, v[12:15] offset:0
	ds_write_b128 v5, v[16:19] offset:2048
	s_waitcnt vmcnt(24)
	v_cvt_pkrtz_f16_f32 v12, v60, v62
	v_cvt_pkrtz_f16_f32 v13, v64, v66
	v_cvt_pkrtz_f16_f32 v14, v68, v70
	v_cvt_pkrtz_f16_f32 v15, v72, v74
	v_cvt_pkrtz_f16_f32 v16, v61, v63
	v_cvt_pkrtz_f16_f32 v17, v65, v67
	v_cvt_pkrtz_f16_f32 v18, v69, v71
	v_cvt_pkrtz_f16_f32 v19, v73, v75
	s_mov_b32 s40, 0x1210d0
	s_mov_b32 s41, 0x142d60
	s_mov_b32 s42, 0x1649f0
	s_mov_b32 s43, 0x186680
	s_mov_b32 s44, 0x1a8310
	s_mov_b32 s45, 0x1c9fa0
	s_mov_b32 s46, 0x1ebc30
	s_mov_b32 s47, 0x20d8c0
	buffer_load_dwordx2 v[60:61], v3, s[4:7], s40 offen nt
	buffer_load_dwordx2 v[62:63], v3, s[4:7], s41 offen nt
	buffer_load_dwordx2 v[64:65], v3, s[4:7], s42 offen nt
	buffer_load_dwordx2 v[66:67], v3, s[4:7], s43 offen nt
	buffer_load_dwordx2 v[68:69], v3, s[4:7], s44 offen nt
	buffer_load_dwordx2 v[70:71], v3, s[4:7], s45 offen nt
	buffer_load_dwordx2 v[72:73], v3, s[4:7], s46 offen nt
	buffer_load_dwordx2 v[74:75], v3, s[4:7], s47 offen nt
	ds_write_b128 v5, v[12:15] offset:256
	ds_write_b128 v5, v[16:19] offset:2304
	s_waitcnt vmcnt(24)
	v_cvt_pkrtz_f16_f32 v12, v76, v78
	v_cvt_pkrtz_f16_f32 v13, v80, v82
	v_cvt_pkrtz_f16_f32 v14, v84, v86
	v_cvt_pkrtz_f16_f32 v15, v88, v90
	v_cvt_pkrtz_f16_f32 v16, v77, v79
	v_cvt_pkrtz_f16_f32 v17, v81, v83
	v_cvt_pkrtz_f16_f32 v18, v85, v87
	v_cvt_pkrtz_f16_f32 v19, v89, v91
	s_mov_b32 s40, 0x22f550
	s_mov_b32 s41, 0x2511e0
	s_mov_b32 s42, 0x272e70
	s_mov_b32 s43, 0x294b00
	s_mov_b32 s44, 0x2b6790
	s_mov_b32 s45, 0x2d8420
	s_mov_b32 s46, 0x2fa0b0
	s_mov_b32 s47, 0x31bd40
	buffer_load_dwordx2 v[76:77], v3, s[4:7], s40 offen nt
	buffer_load_dwordx2 v[78:79], v3, s[4:7], s41 offen nt
	buffer_load_dwordx2 v[80:81], v3, s[4:7], s42 offen nt
	buffer_load_dwordx2 v[82:83], v3, s[4:7], s43 offen nt
	buffer_load_dwordx2 v[84:85], v3, s[4:7], s44 offen nt
	buffer_load_dwordx2 v[86:87], v3, s[4:7], s45 offen nt
	buffer_load_dwordx2 v[88:89], v3, s[4:7], s46 offen nt
	buffer_load_dwordx2 v[90:91], v3, s[4:7], s47 offen nt
	ds_write_b128 v5, v[12:15] offset:512
	ds_write_b128 v5, v[16:19] offset:2560
	s_waitcnt vmcnt(24)
	v_cvt_pkrtz_f16_f32 v12, v92, v94
	v_cvt_pkrtz_f16_f32 v13, v96, v98
	v_cvt_pkrtz_f16_f32 v14, v100, v102
	v_cvt_pkrtz_f16_f32 v15, v104, v106
	v_cvt_pkrtz_f16_f32 v16, v93, v95
	v_cvt_pkrtz_f16_f32 v17, v97, v99
	v_cvt_pkrtz_f16_f32 v18, v101, v103
	v_cvt_pkrtz_f16_f32 v19, v105, v107
	s_mov_b32 s40, 0x33d9d0
	s_mov_b32 s41, 0x35f660
	s_mov_b32 s42, 0x3812f0
	s_mov_b32 s43, 0x3a2f80
	s_mov_b32 s44, 0x3c4c10
	s_mov_b32 s45, 0x3e68a0
	s_mov_b32 s46, 0x408530
	s_mov_b32 s47, 0x42a1c0
	buffer_load_dwordx2 v[92:93], v3, s[4:7], s40 offen nt
	buffer_load_dwordx2 v[94:95], v3, s[4:7], s41 offen nt
	buffer_load_dwordx2 v[96:97], v3, s[4:7], s42 offen nt
	buffer_load_dwordx2 v[98:99], v3, s[4:7], s43 offen nt
	buffer_load_dwordx2 v[100:101], v3, s[4:7], s44 offen nt
	buffer_load_dwordx2 v[102:103], v3, s[4:7], s45 offen nt
	buffer_load_dwordx2 v[104:105], v3, s[4:7], s46 offen nt
	buffer_load_dwordx2 v[106:107], v3, s[4:7], s47 offen nt
	ds_write_b128 v5, v[12:15] offset:768
	ds_write_b128 v5, v[16:19] offset:2816
	s_waitcnt lgkmcnt(0)
	s_barrier
	ds_read_b128 v[12:15], v6 offset:0
	ds_read_b128 v[16:19], v6 offset:2048
	ds_read_b128 v[20:23], v7 offset:0
	ds_read_b128 v[24:27], v7 offset:2048
	ds_read_b128 v[28:31], v8 offset:0
	ds_read_b128 v[32:35], v8 offset:2048
	ds_read_b128 v[36:39], v9 offset:0
	ds_read_b128 v[40:43], v9 offset:2048
	s_waitcnt lgkmcnt(7)
	v_mfma_f32_16x16x32_f16 v[188:191], v[152:155], v[12:15], v[188:191]
	v_mfma_f32_16x16x32_f16 v[220:223], v[112:115], v[12:15], v[220:223]
	s_waitcnt lgkmcnt(6)
	v_mfma_f32_16x16x32_f16 v[192:195], v[156:159], v[16:19], v[192:195]
	v_mfma_f32_16x16x32_f16 v[224:227], v[116:119], v[16:19], v[224:227]
	s_waitcnt lgkmcnt(5)
	v_mfma_f32_16x16x32_f16 v[196:199], v[160:163], v[20:23], v[196:199]
	v_mfma_f32_16x16x32_f16 v[228:231], v[120:123], v[20:23], v[228:231]
	s_waitcnt lgkmcnt(4)
	v_mfma_f32_16x16x32_f16 v[200:203], v[164:167], v[24:27], v[200:203]
	v_mfma_f32_16x16x32_f16 v[232:235], v[124:127], v[24:27], v[232:235]
	s_waitcnt lgkmcnt(3)
	v_mfma_f32_16x16x32_f16 v[204:207], v[168:171], v[28:31], v[204:207]
	v_mfma_f32_16x16x32_f16 v[236:239], v[128:131], v[28:31], v[236:239]
	s_waitcnt lgkmcnt(2)
	v_mfma_f32_16x16x32_f16 v[208:211], v[172:175], v[32:35], v[208:211]
	v_mfma_f32_16x16x32_f16 v[240:243], v[132:135], v[32:35], v[240:243]
	s_waitcnt lgkmcnt(1)
	v_mfma_f32_16x16x32_f16 v[212:215], v[176:179], v[36:39], v[212:215]
	v_mfma_f32_16x16x32_f16 v[244:247], v[136:139], v[36:39], v[244:247]
	s_waitcnt lgkmcnt(0)
	v_mfma_f32_16x16x32_f16 v[216:219], v[180:183], v[40:43], v[216:219]
	v_mfma_f32_16x16x32_f16 v[248:251], v[140:143], v[40:43], v[248:251]
	s_waitcnt vmcnt(24)
	v_cvt_pkrtz_f16_f32 v12, v44, v46
	v_cvt_pkrtz_f16_f32 v13, v48, v50
	v_cvt_pkrtz_f16_f32 v14, v52, v54
	v_cvt_pkrtz_f16_f32 v15, v56, v58
	v_cvt_pkrtz_f16_f32 v16, v45, v47
	v_cvt_pkrtz_f16_f32 v17, v49, v51
	v_cvt_pkrtz_f16_f32 v18, v53, v55
	v_cvt_pkrtz_f16_f32 v19, v57, v59
	s_mov_b32 s40, 0x16860
	s_mov_b32 s41, 0x384f0
	s_mov_b32 s42, 0x5a180
	s_mov_b32 s43, 0x7be10
	s_mov_b32 s44, 0x9daa0
	s_mov_b32 s45, 0xbf730
	s_mov_b32 s46, 0xe13c0
	s_mov_b32 s47, 0x103050
	buffer_load_dwordx2 v[44:45], v3, s[4:7], s40 offen nt
	buffer_load_dwordx2 v[46:47], v3, s[4:7], s41 offen nt
	buffer_load_dwordx2 v[48:49], v3, s[4:7], s42 offen nt
	buffer_load_dwordx2 v[50:51], v3, s[4:7], s43 offen nt
	buffer_load_dwordx2 v[52:53], v3, s[4:7], s44 offen nt
	buffer_load_dwordx2 v[54:55], v3, s[4:7], s45 offen nt
	buffer_load_dwordx2 v[56:57], v3, s[4:7], s46 offen nt
	buffer_load_dwordx2 v[58:59], v3, s[4:7], s47 offen nt
	ds_write_b128 v5, v[12:15] offset:1024
	ds_write_b128 v5, v[16:19] offset:3072
	s_waitcnt vmcnt(24)
	v_cvt_pkrtz_f16_f32 v12, v60, v62
	v_cvt_pkrtz_f16_f32 v13, v64, v66
	v_cvt_pkrtz_f16_f32 v14, v68, v70
	v_cvt_pkrtz_f16_f32 v15, v72, v74
	v_cvt_pkrtz_f16_f32 v16, v61, v63
	v_cvt_pkrtz_f16_f32 v17, v65, v67
	v_cvt_pkrtz_f16_f32 v18, v69, v71
	v_cvt_pkrtz_f16_f32 v19, v73, v75
	s_mov_b32 s40, 0x124ce0
	s_mov_b32 s41, 0x146970
	s_mov_b32 s42, 0x168600
	s_mov_b32 s43, 0x18a290
	s_mov_b32 s44, 0x1abf20
	s_mov_b32 s45, 0x1cdbb0
	s_mov_b32 s46, 0x1ef840
	s_mov_b32 s47, 0x2114d0
	buffer_load_dwordx2 v[60:61], v3, s[4:7], s40 offen nt
	buffer_load_dwordx2 v[62:63], v3, s[4:7], s41 offen nt
	buffer_load_dwordx2 v[64:65], v3, s[4:7], s42 offen nt
	buffer_load_dwordx2 v[66:67], v3, s[4:7], s43 offen nt
	buffer_load_dwordx2 v[68:69], v3, s[4:7], s44 offen nt
	buffer_load_dwordx2 v[70:71], v3, s[4:7], s45 offen nt
	buffer_load_dwordx2 v[72:73], v3, s[4:7], s46 offen nt
	buffer_load_dwordx2 v[74:75], v3, s[4:7], s47 offen nt
	ds_write_b128 v5, v[12:15] offset:1280
	ds_write_b128 v5, v[16:19] offset:3328
	s_waitcnt vmcnt(24)
	v_cvt_pkrtz_f16_f32 v12, v76, v78
	v_cvt_pkrtz_f16_f32 v13, v80, v82
	v_cvt_pkrtz_f16_f32 v14, v84, v86
	v_cvt_pkrtz_f16_f32 v15, v88, v90
	v_cvt_pkrtz_f16_f32 v16, v77, v79
	v_cvt_pkrtz_f16_f32 v17, v81, v83
	v_cvt_pkrtz_f16_f32 v18, v85, v87
	v_cvt_pkrtz_f16_f32 v19, v89, v91
	s_mov_b32 s40, 0x233160
	s_mov_b32 s41, 0x254df0
	s_mov_b32 s42, 0x276a80
	s_mov_b32 s43, 0x298710
	s_mov_b32 s44, 0x2ba3a0
	s_mov_b32 s45, 0x2dc030
	s_mov_b32 s46, 0x2fdcc0
	s_mov_b32 s47, 0x31f950
	buffer_load_dwordx2 v[76:77], v3, s[4:7], s40 offen nt
	buffer_load_dwordx2 v[78:79], v3, s[4:7], s41 offen nt
	buffer_load_dwordx2 v[80:81], v3, s[4:7], s42 offen nt
	buffer_load_dwordx2 v[82:83], v3, s[4:7], s43 offen nt
	buffer_load_dwordx2 v[84:85], v3, s[4:7], s44 offen nt
	buffer_load_dwordx2 v[86:87], v3, s[4:7], s45 offen nt
	buffer_load_dwordx2 v[88:89], v3, s[4:7], s46 offen nt
	buffer_load_dwordx2 v[90:91], v3, s[4:7], s47 offen nt
	ds_write_b128 v5, v[12:15] offset:1536
	ds_write_b128 v5, v[16:19] offset:3584
	s_waitcnt vmcnt(24)
	v_cvt_pkrtz_f16_f32 v12, v92, v94
	v_cvt_pkrtz_f16_f32 v13, v96, v98
	v_cvt_pkrtz_f16_f32 v14, v100, v102
	v_cvt_pkrtz_f16_f32 v15, v104, v106
	v_cvt_pkrtz_f16_f32 v16, v93, v95
	v_cvt_pkrtz_f16_f32 v17, v97, v99
	v_cvt_pkrtz_f16_f32 v18, v101, v103
	v_cvt_pkrtz_f16_f32 v19, v105, v107
	s_mov_b32 s40, 0x3415e0
	s_mov_b32 s41, 0x363270
	s_mov_b32 s42, 0x384f00
	s_mov_b32 s43, 0x3a6b90
	s_mov_b32 s44, 0x3c8820
	s_mov_b32 s45, 0x3ea4b0
	s_mov_b32 s46, 0x40c140
	s_mov_b32 s47, 0x42ddd0
	buffer_load_dwordx2 v[92:93], v3, s[4:7], s40 offen nt
	buffer_load_dwordx2 v[94:95], v3, s[4:7], s41 offen nt
	buffer_load_dwordx2 v[96:97], v3, s[4:7], s42 offen nt
	buffer_load_dwordx2 v[98:99], v3, s[4:7], s43 offen nt
	buffer_load_dwordx2 v[100:101], v3, s[4:7], s44 offen nt
	buffer_load_dwordx2 v[102:103], v3, s[4:7], s45 offen nt
	buffer_load_dwordx2 v[104:105], v3, s[4:7], s46 offen nt
	buffer_load_dwordx2 v[106:107], v3, s[4:7], s47 offen nt
	ds_write_b128 v5, v[12:15] offset:1792
	ds_write_b128 v5, v[16:19] offset:3840
	s_waitcnt lgkmcnt(0)
	s_barrier
	ds_read_b128 v[12:15], v6 offset:1024
	ds_read_b128 v[16:19], v6 offset:3072
	ds_read_b128 v[20:23], v7 offset:1024
	ds_read_b128 v[24:27], v7 offset:3072
	ds_read_b128 v[28:31], v8 offset:1024
	ds_read_b128 v[32:35], v8 offset:3072
	ds_read_b128 v[36:39], v9 offset:1024
	ds_read_b128 v[40:43], v9 offset:3072
	s_waitcnt lgkmcnt(7)
	v_mfma_f32_16x16x32_f16 v[188:191], v[156:159], v[12:15], v[188:191]
	v_mfma_f32_16x16x32_f16 v[220:223], v[116:119], v[12:15], v[220:223]
	s_waitcnt lgkmcnt(6)
	v_mfma_f32_16x16x32_f16 v[192:195], v[160:163], v[16:19], v[192:195]
	v_mfma_f32_16x16x32_f16 v[224:227], v[120:123], v[16:19], v[224:227]
	s_waitcnt lgkmcnt(5)
	v_mfma_f32_16x16x32_f16 v[196:199], v[164:167], v[20:23], v[196:199]
	v_mfma_f32_16x16x32_f16 v[228:231], v[124:127], v[20:23], v[228:231]
	s_waitcnt lgkmcnt(4)
	v_mfma_f32_16x16x32_f16 v[200:203], v[168:171], v[24:27], v[200:203]
	v_mfma_f32_16x16x32_f16 v[232:235], v[128:131], v[24:27], v[232:235]
	s_waitcnt lgkmcnt(3)
	v_mfma_f32_16x16x32_f16 v[204:207], v[172:175], v[28:31], v[204:207]
	v_mfma_f32_16x16x32_f16 v[236:239], v[132:135], v[28:31], v[236:239]
	s_waitcnt lgkmcnt(2)
	v_mfma_f32_16x16x32_f16 v[208:211], v[176:179], v[32:35], v[208:211]
	v_mfma_f32_16x16x32_f16 v[240:243], v[136:139], v[32:35], v[240:243]
	s_waitcnt lgkmcnt(1)
	v_mfma_f32_16x16x32_f16 v[212:215], v[180:183], v[36:39], v[212:215]
	v_mfma_f32_16x16x32_f16 v[244:247], v[140:143], v[36:39], v[244:247]
	s_waitcnt lgkmcnt(0)
	v_mfma_f32_16x16x32_f16 v[216:219], v[184:187], v[40:43], v[216:219]
	v_mfma_f32_16x16x32_f16 v[248:251], v[144:147], v[40:43], v[248:251]
	s_mov_b32 s40, 0x30000
	s_mov_b32 s41, 0x30400
	s_mov_b32 s42, 0x30800
	s_mov_b32 s43, 0x30c00
	s_mov_b32 s44, 0x31000
	buffer_load_dwordx4 v[148:151], v4, s[8:11], s40 offen
	buffer_load_dwordx4 v[152:155], v4, s[8:11], s41 offen
	buffer_load_dwordx4 v[156:159], v4, s[8:11], s42 offen
	buffer_load_dwordx4 v[160:163], v4, s[8:11], s43 offen
	buffer_load_dwordx4 v[164:167], v4, s[8:11], s44 offen
	s_mov_b32 s40, 0x31400
	s_mov_b32 s41, 0x31800
	s_mov_b32 s42, 0x31c00
	s_mov_b32 s43, 0x32000
	s_mov_b32 s44, 0x32400
	buffer_load_dwordx4 v[168:171], v4, s[8:11], s40 offen
	buffer_load_dwordx4 v[172:175], v4, s[8:11], s41 offen
	buffer_load_dwordx4 v[176:179], v4, s[8:11], s42 offen
	buffer_load_dwordx4 v[180:183], v4, s[8:11], s43 offen
	buffer_load_dwordx4 v[184:187], v4, s[8:11], s44 offen
	s_waitcnt vmcnt(34)
	v_cvt_pkrtz_f16_f32 v12, v44, v46
	v_cvt_pkrtz_f16_f32 v13, v48, v50
	v_cvt_pkrtz_f16_f32 v14, v52, v54
	v_cvt_pkrtz_f16_f32 v15, v56, v58
	v_cvt_pkrtz_f16_f32 v16, v45, v47
	v_cvt_pkrtz_f16_f32 v17, v49, v51
	v_cvt_pkrtz_f16_f32 v18, v53, v55
	v_cvt_pkrtz_f16_f32 v19, v57, v59
	s_mov_b32 s40, 0x1a470
	s_mov_b32 s41, 0x3c100
	s_mov_b32 s42, 0x5dd90
	s_mov_b32 s43, 0x7fa20
	s_mov_b32 s44, 0xa16b0
	s_mov_b32 s45, 0xc3340
	s_mov_b32 s46, 0xe4fd0
	s_mov_b32 s47, 0x106c60
	buffer_load_dwordx2 v[44:45], v3, s[4:7], s40 offen nt
	buffer_load_dwordx2 v[46:47], v3, s[4:7], s41 offen nt
	buffer_load_dwordx2 v[48:49], v3, s[4:7], s42 offen nt
	buffer_load_dwordx2 v[50:51], v3, s[4:7], s43 offen nt
	buffer_load_dwordx2 v[52:53], v3, s[4:7], s44 offen nt
	buffer_load_dwordx2 v[54:55], v3, s[4:7], s45 offen nt
	buffer_load_dwordx2 v[56:57], v3, s[4:7], s46 offen nt
	buffer_load_dwordx2 v[58:59], v3, s[4:7], s47 offen nt
	ds_write_b128 v5, v[12:15] offset:0
	ds_write_b128 v5, v[16:19] offset:2048
	s_waitcnt vmcnt(34)
	v_cvt_pkrtz_f16_f32 v12, v60, v62
	v_cvt_pkrtz_f16_f32 v13, v64, v66
	v_cvt_pkrtz_f16_f32 v14, v68, v70
	v_cvt_pkrtz_f16_f32 v15, v72, v74
	v_cvt_pkrtz_f16_f32 v16, v61, v63
	v_cvt_pkrtz_f16_f32 v17, v65, v67
	v_cvt_pkrtz_f16_f32 v18, v69, v71
	v_cvt_pkrtz_f16_f32 v19, v73, v75
	s_mov_b32 s40, 0x1288f0
	s_mov_b32 s41, 0x14a580
	s_mov_b32 s42, 0x16c210
	s_mov_b32 s43, 0x18dea0
	s_mov_b32 s44, 0x1afb30
	s_mov_b32 s45, 0x1d17c0
	s_mov_b32 s46, 0x1f3450
	s_mov_b32 s47, 0x2150e0
	buffer_load_dwordx2 v[60:61], v3, s[4:7], s40 offen nt
	buffer_load_dwordx2 v[62:63], v3, s[4:7], s41 offen nt
	buffer_load_dwordx2 v[64:65], v3, s[4:7], s42 offen nt
	buffer_load_dwordx2 v[66:67], v3, s[4:7], s43 offen nt
	buffer_load_dwordx2 v[68:69], v3, s[4:7], s44 offen nt
	buffer_load_dwordx2 v[70:71], v3, s[4:7], s45 offen nt
	buffer_load_dwordx2 v[72:73], v3, s[4:7], s46 offen nt
	buffer_load_dwordx2 v[74:75], v3, s[4:7], s47 offen nt
	ds_write_b128 v5, v[12:15] offset:256
	ds_write_b128 v5, v[16:19] offset:2304
	s_waitcnt vmcnt(34)
	v_cvt_pkrtz_f16_f32 v12, v76, v78
	v_cvt_pkrtz_f16_f32 v13, v80, v82
	v_cvt_pkrtz_f16_f32 v14, v84, v86
	v_cvt_pkrtz_f16_f32 v15, v88, v90
	v_cvt_pkrtz_f16_f32 v16, v77, v79
	v_cvt_pkrtz_f16_f32 v17, v81, v83
	v_cvt_pkrtz_f16_f32 v18, v85, v87
	v_cvt_pkrtz_f16_f32 v19, v89, v91
	s_mov_b32 s40, 0x236d70
	s_mov_b32 s41, 0x258a00
	s_mov_b32 s42, 0x27a690
	s_mov_b32 s43, 0x29c320
	s_mov_b32 s44, 0x2bdfb0
	s_mov_b32 s45, 0x2dfc40
	s_mov_b32 s46, 0x3018d0
	s_mov_b32 s47, 0x323560
	buffer_load_dwordx2 v[76:77], v3, s[4:7], s40 offen nt
	buffer_load_dwordx2 v[78:79], v3, s[4:7], s41 offen nt
	buffer_load_dwordx2 v[80:81], v3, s[4:7], s42 offen nt
	buffer_load_dwordx2 v[82:83], v3, s[4:7], s43 offen nt
	buffer_load_dwordx2 v[84:85], v3, s[4:7], s44 offen nt
	buffer_load_dwordx2 v[86:87], v3, s[4:7], s45 offen nt
	buffer_load_dwordx2 v[88:89], v3, s[4:7], s46 offen nt
	buffer_load_dwordx2 v[90:91], v3, s[4:7], s47 offen nt
	ds_write_b128 v5, v[12:15] offset:512
	ds_write_b128 v5, v[16:19] offset:2560
	s_waitcnt vmcnt(34)
	v_cvt_pkrtz_f16_f32 v12, v92, v94
	v_cvt_pkrtz_f16_f32 v13, v96, v98
	v_cvt_pkrtz_f16_f32 v14, v100, v102
	v_cvt_pkrtz_f16_f32 v15, v104, v106
	v_cvt_pkrtz_f16_f32 v16, v93, v95
	v_cvt_pkrtz_f16_f32 v17, v97, v99
	v_cvt_pkrtz_f16_f32 v18, v101, v103
	v_cvt_pkrtz_f16_f32 v19, v105, v107
	s_mov_b32 s40, 0x3451f0
	s_mov_b32 s41, 0x366e80
	s_mov_b32 s42, 0x388b10
	s_mov_b32 s43, 0x3aa7a0
	s_mov_b32 s44, 0x3cc430
	s_mov_b32 s45, 0x3ee0c0
	s_mov_b32 s46, 0x40fd50
	s_mov_b32 s47, 0x4319e0
	buffer_load_dwordx2 v[92:93], v3, s[4:7], s40 offen nt
	buffer_load_dwordx2 v[94:95], v3, s[4:7], s41 offen nt
	buffer_load_dwordx2 v[96:97], v3, s[4:7], s42 offen nt
	buffer_load_dwordx2 v[98:99], v3, s[4:7], s43 offen nt
	buffer_load_dwordx2 v[100:101], v3, s[4:7], s44 offen nt
	buffer_load_dwordx2 v[102:103], v3, s[4:7], s45 offen nt
	buffer_load_dwordx2 v[104:105], v3, s[4:7], s46 offen nt
	buffer_load_dwordx2 v[106:107], v3, s[4:7], s47 offen nt
	ds_write_b128 v5, v[12:15] offset:768
	ds_write_b128 v5, v[16:19] offset:2816
	s_waitcnt lgkmcnt(0)
	s_barrier
	ds_read_b128 v[12:15], v6 offset:0
	ds_read_b128 v[16:19], v6 offset:2048
	ds_read_b128 v[20:23], v7 offset:0
	ds_read_b128 v[24:27], v7 offset:2048
	ds_read_b128 v[28:31], v8 offset:0
	ds_read_b128 v[32:35], v8 offset:2048
	ds_read_b128 v[36:39], v9 offset:0
	ds_read_b128 v[40:43], v9 offset:2048
	s_waitcnt vmcnt(32)
	s_waitcnt lgkmcnt(7)
	v_mfma_f32_16x16x32_f16 v[188:191], v[108:111], v[12:15], v[188:191]
	v_mfma_f32_16x16x32_f16 v[220:223], v[148:151], v[12:15], v[220:223]
	s_waitcnt lgkmcnt(6)
	v_mfma_f32_16x16x32_f16 v[192:195], v[112:115], v[16:19], v[192:195]
	v_mfma_f32_16x16x32_f16 v[224:227], v[152:155], v[16:19], v[224:227]
	s_waitcnt lgkmcnt(5)
	v_mfma_f32_16x16x32_f16 v[196:199], v[116:119], v[20:23], v[196:199]
	v_mfma_f32_16x16x32_f16 v[228:231], v[156:159], v[20:23], v[228:231]
	s_waitcnt lgkmcnt(4)
	v_mfma_f32_16x16x32_f16 v[200:203], v[120:123], v[24:27], v[200:203]
	v_mfma_f32_16x16x32_f16 v[232:235], v[160:163], v[24:27], v[232:235]
	s_waitcnt lgkmcnt(3)
	v_mfma_f32_16x16x32_f16 v[204:207], v[124:127], v[28:31], v[204:207]
	v_mfma_f32_16x16x32_f16 v[236:239], v[164:167], v[28:31], v[236:239]
	s_waitcnt lgkmcnt(2)
	v_mfma_f32_16x16x32_f16 v[208:211], v[128:131], v[32:35], v[208:211]
	v_mfma_f32_16x16x32_f16 v[240:243], v[168:171], v[32:35], v[240:243]
	s_waitcnt lgkmcnt(1)
	v_mfma_f32_16x16x32_f16 v[212:215], v[132:135], v[36:39], v[212:215]
	v_mfma_f32_16x16x32_f16 v[244:247], v[172:175], v[36:39], v[244:247]
	s_waitcnt lgkmcnt(0)
	v_mfma_f32_16x16x32_f16 v[216:219], v[136:139], v[40:43], v[216:219]
	v_mfma_f32_16x16x32_f16 v[248:251], v[176:179], v[40:43], v[248:251]
	s_waitcnt vmcnt(24)
	v_cvt_pkrtz_f16_f32 v12, v44, v46
	v_cvt_pkrtz_f16_f32 v13, v48, v50
	v_cvt_pkrtz_f16_f32 v14, v52, v54
	v_cvt_pkrtz_f16_f32 v15, v56, v58
	v_cvt_pkrtz_f16_f32 v16, v45, v47
	v_cvt_pkrtz_f16_f32 v17, v49, v51
	v_cvt_pkrtz_f16_f32 v18, v53, v55
	v_cvt_pkrtz_f16_f32 v19, v57, v59
	s_mov_b32 s40, 0x1e080
	s_mov_b32 s41, 0x3fd10
	s_mov_b32 s42, 0x619a0
	s_mov_b32 s43, 0x83630
	s_mov_b32 s44, 0xa52c0
	s_mov_b32 s45, 0xc6f50
	s_mov_b32 s46, 0xe8be0
	s_mov_b32 s47, 0x10a870
	buffer_load_dwordx2 v[44:45], v3, s[4:7], s40 offen nt
	buffer_load_dwordx2 v[46:47], v3, s[4:7], s41 offen nt
	buffer_load_dwordx2 v[48:49], v3, s[4:7], s42 offen nt
	buffer_load_dwordx2 v[50:51], v3, s[4:7], s43 offen nt
	buffer_load_dwordx2 v[52:53], v3, s[4:7], s44 offen nt
	buffer_load_dwordx2 v[54:55], v3, s[4:7], s45 offen nt
	buffer_load_dwordx2 v[56:57], v3, s[4:7], s46 offen nt
	buffer_load_dwordx2 v[58:59], v3, s[4:7], s47 offen nt
	ds_write_b128 v5, v[12:15] offset:1024
	ds_write_b128 v5, v[16:19] offset:3072
	s_waitcnt vmcnt(24)
	v_cvt_pkrtz_f16_f32 v12, v60, v62
	v_cvt_pkrtz_f16_f32 v13, v64, v66
	v_cvt_pkrtz_f16_f32 v14, v68, v70
	v_cvt_pkrtz_f16_f32 v15, v72, v74
	v_cvt_pkrtz_f16_f32 v16, v61, v63
	v_cvt_pkrtz_f16_f32 v17, v65, v67
	v_cvt_pkrtz_f16_f32 v18, v69, v71
	v_cvt_pkrtz_f16_f32 v19, v73, v75
	s_mov_b32 s40, 0x12c500
	s_mov_b32 s41, 0x14e190
	s_mov_b32 s42, 0x16fe20
	s_mov_b32 s43, 0x191ab0
	s_mov_b32 s44, 0x1b3740
	s_mov_b32 s45, 0x1d53d0
	s_mov_b32 s46, 0x1f7060
	s_mov_b32 s47, 0x218cf0
	buffer_load_dwordx2 v[60:61], v3, s[4:7], s40 offen nt
	buffer_load_dwordx2 v[62:63], v3, s[4:7], s41 offen nt
	buffer_load_dwordx2 v[64:65], v3, s[4:7], s42 offen nt
	buffer_load_dwordx2 v[66:67], v3, s[4:7], s43 offen nt
	buffer_load_dwordx2 v[68:69], v3, s[4:7], s44 offen nt
	buffer_load_dwordx2 v[70:71], v3, s[4:7], s45 offen nt
	buffer_load_dwordx2 v[72:73], v3, s[4:7], s46 offen nt
	buffer_load_dwordx2 v[74:75], v3, s[4:7], s47 offen nt
	ds_write_b128 v5, v[12:15] offset:1280
	ds_write_b128 v5, v[16:19] offset:3328
	s_waitcnt vmcnt(24)
	v_cvt_pkrtz_f16_f32 v12, v76, v78
	v_cvt_pkrtz_f16_f32 v13, v80, v82
	v_cvt_pkrtz_f16_f32 v14, v84, v86
	v_cvt_pkrtz_f16_f32 v15, v88, v90
	v_cvt_pkrtz_f16_f32 v16, v77, v79
	v_cvt_pkrtz_f16_f32 v17, v81, v83
	v_cvt_pkrtz_f16_f32 v18, v85, v87
	v_cvt_pkrtz_f16_f32 v19, v89, v91
	s_mov_b32 s40, 0x23a980
	s_mov_b32 s41, 0x25c610
	s_mov_b32 s42, 0x27e2a0
	s_mov_b32 s43, 0x29ff30
	s_mov_b32 s44, 0x2c1bc0
	s_mov_b32 s45, 0x2e3850
	s_mov_b32 s46, 0x3054e0
	s_mov_b32 s47, 0x327170
	buffer_load_dwordx2 v[76:77], v3, s[4:7], s40 offen nt
	buffer_load_dwordx2 v[78:79], v3, s[4:7], s41 offen nt
	buffer_load_dwordx2 v[80:81], v3, s[4:7], s42 offen nt
	buffer_load_dwordx2 v[82:83], v3, s[4:7], s43 offen nt
	buffer_load_dwordx2 v[84:85], v3, s[4:7], s44 offen nt
	buffer_load_dwordx2 v[86:87], v3, s[4:7], s45 offen nt
	buffer_load_dwordx2 v[88:89], v3, s[4:7], s46 offen nt
	buffer_load_dwordx2 v[90:91], v3, s[4:7], s47 offen nt
	ds_write_b128 v5, v[12:15] offset:1536
	ds_write_b128 v5, v[16:19] offset:3584
	s_waitcnt vmcnt(24)
	v_cvt_pkrtz_f16_f32 v12, v92, v94
	v_cvt_pkrtz_f16_f32 v13, v96, v98
	v_cvt_pkrtz_f16_f32 v14, v100, v102
	v_cvt_pkrtz_f16_f32 v15, v104, v106
	v_cvt_pkrtz_f16_f32 v16, v93, v95
	v_cvt_pkrtz_f16_f32 v17, v97, v99
	v_cvt_pkrtz_f16_f32 v18, v101, v103
	v_cvt_pkrtz_f16_f32 v19, v105, v107
	s_mov_b32 s40, 0x348e00
	s_mov_b32 s41, 0x36aa90
	s_mov_b32 s42, 0x38c720
	s_mov_b32 s43, 0x3ae3b0
	s_mov_b32 s44, 0x3d0040
	s_mov_b32 s45, 0x3f1cd0
	s_mov_b32 s46, 0x413960
	s_mov_b32 s47, 0x4355f0
	buffer_load_dwordx2 v[92:93], v3, s[4:7], s40 offen nt
	buffer_load_dwordx2 v[94:95], v3, s[4:7], s41 offen nt
	buffer_load_dwordx2 v[96:97], v3, s[4:7], s42 offen nt
	buffer_load_dwordx2 v[98:99], v3, s[4:7], s43 offen nt
	buffer_load_dwordx2 v[100:101], v3, s[4:7], s44 offen nt
	buffer_load_dwordx2 v[102:103], v3, s[4:7], s45 offen nt
	buffer_load_dwordx2 v[104:105], v3, s[4:7], s46 offen nt
	buffer_load_dwordx2 v[106:107], v3, s[4:7], s47 offen nt
	ds_write_b128 v5, v[12:15] offset:1792
	ds_write_b128 v5, v[16:19] offset:3840
	s_waitcnt lgkmcnt(0)
	s_barrier
	ds_read_b128 v[12:15], v6 offset:1024
	ds_read_b128 v[16:19], v6 offset:3072
	ds_read_b128 v[20:23], v7 offset:1024
	ds_read_b128 v[24:27], v7 offset:3072
	ds_read_b128 v[28:31], v8 offset:1024
	ds_read_b128 v[32:35], v8 offset:3072
	ds_read_b128 v[36:39], v9 offset:1024
	ds_read_b128 v[40:43], v9 offset:3072
	s_waitcnt lgkmcnt(7)
	v_mfma_f32_16x16x32_f16 v[188:191], v[112:115], v[12:15], v[188:191]
	v_mfma_f32_16x16x32_f16 v[220:223], v[152:155], v[12:15], v[220:223]
	s_waitcnt lgkmcnt(6)
	v_mfma_f32_16x16x32_f16 v[192:195], v[116:119], v[16:19], v[192:195]
	v_mfma_f32_16x16x32_f16 v[224:227], v[156:159], v[16:19], v[224:227]
	s_waitcnt lgkmcnt(5)
	v_mfma_f32_16x16x32_f16 v[196:199], v[120:123], v[20:23], v[196:199]
	v_mfma_f32_16x16x32_f16 v[228:231], v[160:163], v[20:23], v[228:231]
	s_waitcnt lgkmcnt(4)
	v_mfma_f32_16x16x32_f16 v[200:203], v[124:127], v[24:27], v[200:203]
	v_mfma_f32_16x16x32_f16 v[232:235], v[164:167], v[24:27], v[232:235]
	s_waitcnt lgkmcnt(3)
	v_mfma_f32_16x16x32_f16 v[204:207], v[128:131], v[28:31], v[204:207]
	v_mfma_f32_16x16x32_f16 v[236:239], v[168:171], v[28:31], v[236:239]
	s_waitcnt lgkmcnt(2)
	v_mfma_f32_16x16x32_f16 v[208:211], v[132:135], v[32:35], v[208:211]
	v_mfma_f32_16x16x32_f16 v[240:243], v[172:175], v[32:35], v[240:243]
	s_waitcnt lgkmcnt(1)
	v_mfma_f32_16x16x32_f16 v[212:215], v[136:139], v[36:39], v[212:215]
	v_mfma_f32_16x16x32_f16 v[244:247], v[176:179], v[36:39], v[244:247]
	s_waitcnt lgkmcnt(0)
	v_mfma_f32_16x16x32_f16 v[216:219], v[140:143], v[40:43], v[216:219]
	v_mfma_f32_16x16x32_f16 v[248:251], v[180:183], v[40:43], v[248:251]
	s_waitcnt vmcnt(24)
	v_cvt_pkrtz_f16_f32 v12, v44, v46
	v_cvt_pkrtz_f16_f32 v13, v48, v50
	v_cvt_pkrtz_f16_f32 v14, v52, v54
	v_cvt_pkrtz_f16_f32 v15, v56, v58
	v_cvt_pkrtz_f16_f32 v16, v45, v47
	v_cvt_pkrtz_f16_f32 v17, v49, v51
	v_cvt_pkrtz_f16_f32 v18, v53, v55
	v_cvt_pkrtz_f16_f32 v19, v57, v59
	ds_write_b128 v5, v[12:15] offset:0
	ds_write_b128 v5, v[16:19] offset:2048
	s_waitcnt vmcnt(16)
	v_cvt_pkrtz_f16_f32 v12, v60, v62
	v_cvt_pkrtz_f16_f32 v13, v64, v66
	v_cvt_pkrtz_f16_f32 v14, v68, v70
	v_cvt_pkrtz_f16_f32 v15, v72, v74
	v_cvt_pkrtz_f16_f32 v16, v61, v63
	v_cvt_pkrtz_f16_f32 v17, v65, v67
	v_cvt_pkrtz_f16_f32 v18, v69, v71
	v_cvt_pkrtz_f16_f32 v19, v73, v75
	ds_write_b128 v5, v[12:15] offset:256
	ds_write_b128 v5, v[16:19] offset:2304
	s_waitcnt vmcnt(8)
	v_cvt_pkrtz_f16_f32 v12, v76, v78
	v_cvt_pkrtz_f16_f32 v13, v80, v82
	v_cvt_pkrtz_f16_f32 v14, v84, v86
	v_cvt_pkrtz_f16_f32 v15, v88, v90
	v_cvt_pkrtz_f16_f32 v16, v77, v79
	v_cvt_pkrtz_f16_f32 v17, v81, v83
	v_cvt_pkrtz_f16_f32 v18, v85, v87
	v_cvt_pkrtz_f16_f32 v19, v89, v91
	ds_write_b128 v5, v[12:15] offset:512
	ds_write_b128 v5, v[16:19] offset:2560
	s_waitcnt vmcnt(0)
	v_cvt_pkrtz_f16_f32 v12, v92, v94
	v_cvt_pkrtz_f16_f32 v13, v96, v98
	v_cvt_pkrtz_f16_f32 v14, v100, v102
	v_cvt_pkrtz_f16_f32 v15, v104, v106
	v_cvt_pkrtz_f16_f32 v16, v93, v95
	v_cvt_pkrtz_f16_f32 v17, v97, v99
	v_cvt_pkrtz_f16_f32 v18, v101, v103
	v_cvt_pkrtz_f16_f32 v19, v105, v107
	ds_write_b128 v5, v[12:15] offset:768
	ds_write_b128 v5, v[16:19] offset:2816
	s_waitcnt lgkmcnt(0)
	s_barrier
	ds_read_b128 v[12:15], v6 offset:0
	ds_read_b128 v[16:19], v6 offset:2048
	ds_read_b128 v[20:23], v7 offset:0
	ds_read_b128 v[24:27], v7 offset:2048
	ds_read_b128 v[28:31], v8 offset:0
	ds_read_b128 v[32:35], v8 offset:2048
	ds_read_b128 v[36:39], v9 offset:0
	ds_read_b128 v[40:43], v9 offset:2048
	s_waitcnt lgkmcnt(7)
	v_mfma_f32_16x16x32_f16 v[188:191], v[116:119], v[12:15], v[188:191]
	v_mfma_f32_16x16x32_f16 v[220:223], v[156:159], v[12:15], v[220:223]
	s_waitcnt lgkmcnt(6)
	v_mfma_f32_16x16x32_f16 v[192:195], v[120:123], v[16:19], v[192:195]
	v_mfma_f32_16x16x32_f16 v[224:227], v[160:163], v[16:19], v[224:227]
	s_waitcnt lgkmcnt(5)
	v_mfma_f32_16x16x32_f16 v[196:199], v[124:127], v[20:23], v[196:199]
	v_mfma_f32_16x16x32_f16 v[228:231], v[164:167], v[20:23], v[228:231]
	s_waitcnt lgkmcnt(4)
	v_mfma_f32_16x16x32_f16 v[200:203], v[128:131], v[24:27], v[200:203]
	v_mfma_f32_16x16x32_f16 v[232:235], v[168:171], v[24:27], v[232:235]
	s_waitcnt lgkmcnt(3)
	v_mfma_f32_16x16x32_f16 v[204:207], v[132:135], v[28:31], v[204:207]
	v_mfma_f32_16x16x32_f16 v[236:239], v[172:175], v[28:31], v[236:239]
	s_waitcnt lgkmcnt(2)
	v_mfma_f32_16x16x32_f16 v[208:211], v[136:139], v[32:35], v[208:211]
	v_mfma_f32_16x16x32_f16 v[240:243], v[176:179], v[32:35], v[240:243]
	s_waitcnt lgkmcnt(1)
	v_mfma_f32_16x16x32_f16 v[212:215], v[140:143], v[36:39], v[212:215]
	v_mfma_f32_16x16x32_f16 v[244:247], v[180:183], v[36:39], v[244:247]
	s_waitcnt lgkmcnt(0)
	v_mfma_f32_16x16x32_f16 v[216:219], v[144:147], v[40:43], v[216:219]
	v_mfma_f32_16x16x32_f16 v[248:251], v[184:187], v[40:43], v[248:251]
	s_nop 7
	s_nop 3
	v_and_b32_e32 v10, 1, v0
	v_cmp_eq_u32_e32 vcc, 1, v10
	s_nop 1
	v_cndmask_b32_e32 v188, v188, v220, vcc
	v_cndmask_b32_e32 v189, v189, v221, vcc
	v_cndmask_b32_e32 v190, v190, v222, vcc
	v_cndmask_b32_e32 v191, v191, v223, vcc
	v_cndmask_b32_e32 v192, v192, v224, vcc
	v_cndmask_b32_e32 v193, v193, v225, vcc
	v_cndmask_b32_e32 v194, v194, v226, vcc
	v_cndmask_b32_e32 v195, v195, v227, vcc
	v_cndmask_b32_e32 v196, v196, v228, vcc
	v_cndmask_b32_e32 v197, v197, v229, vcc
	v_cndmask_b32_e32 v198, v198, v230, vcc
	v_cndmask_b32_e32 v199, v199, v231, vcc
	v_cndmask_b32_e32 v200, v200, v232, vcc
	v_cndmask_b32_e32 v201, v201, v233, vcc
	v_cndmask_b32_e32 v202, v202, v234, vcc
	v_cndmask_b32_e32 v203, v203, v235, vcc
	v_cndmask_b32_e32 v204, v204, v236, vcc
	v_cndmask_b32_e32 v205, v205, v237, vcc
	v_cndmask_b32_e32 v206, v206, v238, vcc
	v_cndmask_b32_e32 v207, v207, v239, vcc
	v_cndmask_b32_e32 v208, v208, v240, vcc
	v_cndmask_b32_e32 v209, v209, v241, vcc
	v_cndmask_b32_e32 v210, v210, v242, vcc
	v_cndmask_b32_e32 v211, v211, v243, vcc
	v_cndmask_b32_e32 v212, v212, v244, vcc
	v_cndmask_b32_e32 v213, v213, v245, vcc
	v_cndmask_b32_e32 v214, v214, v246, vcc
	v_cndmask_b32_e32 v215, v215, v247, vcc
	v_cndmask_b32_e32 v216, v216, v248, vcc
	v_cndmask_b32_e32 v217, v217, v249, vcc
	v_cndmask_b32_e32 v218, v218, v250, vcc
	v_cndmask_b32_e32 v219, v219, v251, vcc
	s_barrier
	v_lshrrev_b32_e32 v10, 4, v2
	v_lshlrev_b32_e32 v10, 6, v10
	v_and_b32_e32 v12, 15, v2
	v_add_u32_e32 v10, v10, v12
	v_mul_u32_u24_e32 v10, 0x108, v10
	v_lshl_add_u32 v10, v1, 5, v10
	ds_write_b32 v10, v188 offset:0
	ds_write_b32 v10, v189 offset:4224
	ds_write_b32 v10, v190 offset:8448
	ds_write_b32 v10, v191 offset:12672
	ds_write_b32 v10, v192 offset:4
	ds_write_b32 v10, v193 offset:4228
	ds_write_b32 v10, v194 offset:8452
	ds_write_b32 v10, v195 offset:12676
	s_waitcnt lgkmcnt(4)
	ds_write_b32 v10, v196 offset:8
	ds_write_b32 v10, v197 offset:4232
	ds_write_b32 v10, v198 offset:8456
	ds_write_b32 v10, v199 offset:12680
	ds_write_b32 v10, v200 offset:12
	ds_write_b32 v10, v201 offset:4236
	ds_write_b32 v10, v202 offset:8460
	ds_write_b32 v10, v203 offset:12684
	s_waitcnt lgkmcnt(4)
	ds_write_b32 v10, v204 offset:16
	ds_write_b32 v10, v205 offset:4240
	ds_write_b32 v10, v206 offset:8464
	ds_write_b32 v10, v207 offset:12688
	ds_write_b32 v10, v208 offset:20
	ds_write_b32 v10, v209 offset:4244
	ds_write_b32 v10, v210 offset:8468
	ds_write_b32 v10, v211 offset:12692
	s_waitcnt lgkmcnt(4)
	ds_write_b32 v10, v212 offset:24
	ds_write_b32 v10, v213 offset:4248
	ds_write_b32 v10, v214 offset:8472
	ds_write_b32 v10, v215 offset:12696
	ds_write_b32 v10, v216 offset:28
	ds_write_b32 v10, v217 offset:4252
	ds_write_b32 v10, v218 offset:8476
	ds_write_b32 v10, v219 offset:12700
	s_waitcnt lgkmcnt(0)
	s_barrier
	v_lshrrev_b32_e32 v12, 5, v0
	v_mul_u32_u24_e32 v12, 0x108, v12
	v_and_b32_e32 v13, 31, v0
	v_lshl_add_u32 v12, v13, 3, v12
	ds_read_b64 v[44:45], v12 offset:0
	ds_read_b64 v[46:47], v12 offset:4224
	ds_read_b64 v[48:49], v12 offset:8448
	ds_read_b64 v[50:51], v12 offset:12672
	ds_read_b64 v[52:53], v12 offset:16896
	ds_read_b64 v[54:55], v12 offset:21120
	ds_read_b64 v[56:57], v12 offset:25344
	ds_read_b64 v[58:59], v12 offset:29568
	s_waitcnt lgkmcnt(7)
	v_add_f32_e32 v44, v252, v44
	v_add_f32_e32 v45, v253, v45
	s_mov_b32 s40, 0x0
	buffer_store_dwordx2 v[44:45], v11, s[32:35], s40 offen nt
	s_waitcnt lgkmcnt(6)
	v_add_f32_e32 v46, v252, v46
	v_add_f32_e32 v47, v253, v47
	s_mov_b32 s41, 0xf0400
	buffer_store_dwordx2 v[46:47], v11, s[32:35], s41 offen nt
	s_waitcnt lgkmcnt(5)
	v_add_f32_e32 v48, v252, v48
	v_add_f32_e32 v49, v253, v49
	s_mov_b32 s42, 0x1e0800
	buffer_store_dwordx2 v[48:49], v11, s[32:35], s42 offen nt
	s_waitcnt lgkmcnt(4)
	v_add_f32_e32 v50, v252, v50
	v_add_f32_e32 v51, v253, v51
	s_mov_b32 s43, 0x2d0c00
	buffer_store_dwordx2 v[50:51], v11, s[32:35], s43 offen nt
	s_waitcnt lgkmcnt(3)
	v_add_f32_e32 v52, v252, v52
	v_add_f32_e32 v53, v253, v53
	s_mov_b32 s44, 0x3c1000
	buffer_store_dwordx2 v[52:53], v11, s[32:35], s44 offen nt
	s_waitcnt lgkmcnt(2)
	v_add_f32_e32 v54, v252, v54
	v_add_f32_e32 v55, v253, v55
	s_mov_b32 s45, 0x4b1400
	buffer_store_dwordx2 v[54:55], v11, s[32:35], s45 offen nt
	s_waitcnt lgkmcnt(1)
	v_add_f32_e32 v56, v252, v56
	v_add_f32_e32 v57, v253, v57
	s_mov_b32 s46, 0x5a1800
	buffer_store_dwordx2 v[56:57], v11, s[32:35], s46 offen nt
	s_waitcnt lgkmcnt(0)
	v_add_f32_e32 v58, v252, v58
	v_add_f32_e32 v59, v253, v59
	s_mov_b32 s47, 0x691c00
	buffer_store_dwordx2 v[58:59], v11, s[32:35], s47 offen nt
	ds_read_b64 v[60:61], v12 offset:33792
	ds_read_b64 v[62:63], v12 offset:38016
	ds_read_b64 v[64:65], v12 offset:42240
	ds_read_b64 v[66:67], v12 offset:46464
	ds_read_b64 v[68:69], v12 offset:50688
	ds_read_b64 v[70:71], v12 offset:54912
	ds_read_b64 v[72:73], v12 offset:59136
	ds_read_b64 v[74:75], v12 offset:63360
	s_waitcnt lgkmcnt(7)
	v_add_f32_e32 v60, v252, v60
	v_add_f32_e32 v61, v253, v61
	s_mov_b32 s40, 0x782000
	buffer_store_dwordx2 v[60:61], v11, s[32:35], s40 offen nt
	s_waitcnt lgkmcnt(6)
	v_add_f32_e32 v62, v252, v62
	v_add_f32_e32 v63, v253, v63
	s_mov_b32 s41, 0x872400
	buffer_store_dwordx2 v[62:63], v11, s[32:35], s41 offen nt
	s_waitcnt lgkmcnt(5)
	v_add_f32_e32 v64, v252, v64
	v_add_f32_e32 v65, v253, v65
	s_mov_b32 s42, 0x962800
	buffer_store_dwordx2 v[64:65], v11, s[32:35], s42 offen nt
	s_waitcnt lgkmcnt(4)
	v_add_f32_e32 v66, v252, v66
	v_add_f32_e32 v67, v253, v67
	s_mov_b32 s43, 0xa52c00
	buffer_store_dwordx2 v[66:67], v11, s[32:35], s43 offen nt
	s_waitcnt lgkmcnt(3)
	v_add_f32_e32 v68, v252, v68
	v_add_f32_e32 v69, v253, v69
	s_mov_b32 s44, 0xb43000
	buffer_store_dwordx2 v[68:69], v11, s[32:35], s44 offen nt
	s_waitcnt lgkmcnt(2)
	v_add_f32_e32 v70, v252, v70
	v_add_f32_e32 v71, v253, v71
	s_mov_b32 s45, 0xc33400
	buffer_store_dwordx2 v[70:71], v11, s[32:35], s45 offen nt
	s_waitcnt lgkmcnt(1)
	v_add_f32_e32 v72, v252, v72
	v_add_f32_e32 v73, v253, v73
	s_mov_b32 s46, 0xd23800
	buffer_store_dwordx2 v[72:73], v11, s[32:35], s46 offen nt
	s_waitcnt lgkmcnt(0)
	v_add_f32_e32 v74, v252, v74
	v_add_f32_e32 v75, v253, v75
	s_mov_b32 s47, 0xe13c00
	buffer_store_dwordx2 v[74:75], v11, s[32:35], s47 offen nt
	s_endpgm
